# speedup vs baseline: 1.1070x; 1.0244x over previous
.LBB3_35:
	s_andn2_b64 vcc, exec, s[2:3]
	s_cbranch_vccnz .LBB3_39
	s_waitcnt vmcnt(4)
	v_ashrrev_i32_e32 v81, 31, v80
	v_lshl_add_u64 v[2:3], v[80:81], 3, s[20:21]
	v_add_co_u32_e32 v2, vcc, 0x48000, v2
	s_movk_i32 s8, 0x620
	s_nop 0
	v_addc_co_u32_e32 v3, vcc, 0, v3, vcc
	global_load_dwordx2 v[82:83], v[2:3], off
	v_and_b32_e32 v2, 0x70, v7
	v_bitop3_b32 v2, v0, v2, 48 bitop3:0x6c
	s_waitcnt vmcnt(4)
	v_mad_u64_u32 v[64:65], s[6:7], v9, s8, v[2:3]
	v_lshrrev_b32_e32 v3, 4, v92
	v_bitop3_b32 v3, v3, v0, 4 bitop3:0x36
	v_lshlrev_b32_e32 v3, 4, v3
	v_and_b32_e32 v4, 0x70, v3
	s_waitcnt vmcnt(3)
	v_mad_u64_u32 v[66:67], s[6:7], v8, s8, v[4:5]
	s_waitcnt vmcnt(2)
	v_mad_u64_u32 v[68:69], s[6:7], v6, s8, v[2:3]
	s_waitcnt vmcnt(1)
	v_mad_u64_u32 v[70:71], s[6:7], v1, s8, v[4:5]
	v_lshrrev_b32_e32 v85, 5, v92
	v_bfe_u32 v2, v0, 1, 3
	s_mov_b64 s[6:7], 0x1800
	s_add_u32 s4, s20, 0x4000000
	v_bitop3_b32 v32, v85, v2, 2 bitop3:0x36
	v_bitop3_b32 v33, v85, v2, 4 bitop3:0x36
	v_bitop3_b32 v34, v85, v2, 6 bitop3:0x36
	v_lshl_add_u64 v[2:3], v[86:87], 0, s[6:7]
	s_addc_u32 s5, s21, 0
	s_lshl_b32 s2, s27, 12
	s_addk_i32 s2, 0x6000
	v_lshrrev_b32_e32 v1, 1, v0
	v_or_b32_e32 v81, s2, v84
	v_lshlrev_b32_e32 v0, 7, v0
	v_and_b32_e32 v8, 0xf80, v0
	v_lshlrev_b32_e32 v9, 4, v32
	v_bitop3_b32 v1, v85, v1, 7 bitop3:0x78
	v_or3_b32 v96, s2, v9, v8
	v_lshlrev_b32_e32 v9, 4, v33
	v_lshlrev_b32_e32 v1, 4, v1
	v_or3_b32 v97, s2, v9, v8
	v_lshlrev_b32_e32 v9, 4, v34
	v_or3_b32 v95, s2, v1, v8
	v_or3_b32 v94, s2, v9, v8
	v_add_u32_e32 v98, 0x103c0, v84
	global_load_dwordx4 v[116:119], v64, s[4:5] offset:0
	global_load_dwordx4 v[120:123], v66, s[4:5] offset:0
	global_load_dwordx4 v[124:127], v68, s[4:5] offset:0
	global_load_dwordx4 v[128:131], v70, s[4:5] offset:0
	global_load_dwordx4 v[132:135], v64, s[4:5] offset:128
	global_load_dwordx4 v[136:139], v66, s[4:5] offset:128
	global_load_dwordx4 v[140:143], v68, s[4:5] offset:128
	global_load_dwordx4 v[144:147], v70, s[4:5] offset:128
	global_load_dwordx4 v[148:151], v64, s[4:5] offset:256
	global_load_dwordx4 v[152:155], v66, s[4:5] offset:256
	global_load_dwordx4 v[156:159], v68, s[4:5] offset:256
	global_load_dwordx4 v[72:75], v70, s[4:5] offset:256
	s_add_u32 m0, s46, 0x0
	s_nop 0
	global_load_lds_dwordx4 v84, s[40:41]
	s_add_u32 m0, s47, 0x0
	s_nop 0
	global_load_lds_dwordx4 v84, s[42:43]
	s_add_u32 m0, s48, 0x0
	s_nop 0
	global_load_lds_dwordx4 v84, s[44:45]
	s_add_u32 m0, s46, 0x3000
	s_add_u32 s40, s40, 0x1800
	s_addc_u32 s41, s41, 0
	global_load_lds_dwordx4 v84, s[40:41]
	s_add_u32 m0, s47, 0x3000
	s_add_u32 s42, s42, 0x1800
	s_addc_u32 s43, s43, 0
	global_load_lds_dwordx4 v84, s[42:43]
	s_add_u32 m0, s48, 0x3000
	s_add_u32 s44, s44, 0x1800
	s_addc_u32 s45, s45, 0
	global_load_lds_dwordx4 v84, s[44:45]
	s_add_u32 m0, s46, 0xd3c0
	s_add_u32 s40, s40, 0x1800
	s_addc_u32 s41, s41, 0
	global_load_lds_dwordx4 v84, s[40:41]
	s_add_u32 m0, s47, 0xd3c0
	s_add_u32 s42, s42, 0x1800
	s_addc_u32 s43, s43, 0
	global_load_lds_dwordx4 v84, s[42:43]
	s_add_u32 m0, s48, 0xd3c0
	s_add_u32 s44, s44, 0x1800
	s_addc_u32 s45, s45, 0
	global_load_lds_dwordx4 v84, s[44:45]
	s_add_u32 m0, s46, 0x103c0
	s_add_u32 s40, s40, 0x1800
	s_addc_u32 s41, s41, 0
	global_load_lds_dwordx4 v84, s[40:41]
	s_add_u32 m0, s47, 0x103c0
	s_add_u32 s42, s42, 0x1800
	s_addc_u32 s43, s43, 0
	global_load_lds_dwordx4 v84, s[42:43]
	s_add_u32 m0, s48, 0x103c0
	s_add_u32 s44, s44, 0x1800
	s_addc_u32 s45, s45, 0
	global_load_lds_dwordx4 v84, s[44:45]
	s_waitcnt vmcnt(20)
	ds_write_b128 v81, v[116:119]
	ds_write_b128 v81, v[120:123] offset:1024
	ds_write_b128 v81, v[124:127] offset:2048
	ds_write_b128 v81, v[128:131] offset:3072
	ds_read_b128 v[52:55], v95
	ds_read_b128 v[56:59], v96
	ds_read_b128 v[60:63], v97
	ds_read_b128 v[0:3], v94
	global_load_dwordx4 v[116:119], v64, s[4:5] offset:384
	global_load_dwordx4 v[120:123], v66, s[4:5] offset:384
	global_load_dwordx4 v[124:127], v68, s[4:5] offset:384
	global_load_dwordx4 v[128:131], v70, s[4:5] offset:384
	s_waitcnt vmcnt(13)
	s_waitcnt lgkmcnt(0)
	s_barrier
	ds_read_b128 v[4:7], v84 offset:0
	ds_read_b128 v[8:11], v84 offset:1024
	ds_read_b128 v[12:15], v84 offset:2048
	ds_read_b128 v[16:19], v84 offset:3072
	ds_read_b128 v[20:23], v84 offset:4096
	ds_read_b128 v[24:27], v84 offset:5120
	ds_read_b128 v[28:31], v84 offset:6144
	ds_read_b128 v[32:35], v84 offset:7168
	ds_read_b128 v[36:39], v84 offset:8192
	ds_read_b128 v[40:43], v84 offset:9216
	ds_read_b128 v[44:47], v84 offset:10240
	ds_read_b128 v[48:51], v84 offset:11264
	s_waitcnt lgkmcnt(6)
	v_mfma_f32_32x32x16_f16 a[80:95], v[4:7], v[52:55], 0
	v_mfma_f32_32x32x16_f16 a[64:79], v[8:11], v[52:55], 0
	v_mfma_f32_32x32x16_f16 a[48:63], v[12:15], v[52:55], 0
	s_waitcnt vmcnt(10)
	s_waitcnt lgkmcnt(0)
	s_barrier
	ds_read_b128 v[4:7], v84 offset:12288
	ds_read_b128 v[8:11], v84 offset:13312
	ds_read_b128 v[12:15], v84 offset:14336
	v_mfma_f32_32x32x16_f16 a[32:47], v[16:19], v[52:55], 0
	ds_read_b128 v[16:19], v84 offset:15360
	v_mfma_f32_32x32x16_f16 a[16:31], v[20:23], v[52:55], 0
	ds_read_b128 v[20:23], v84 offset:16384
	v_mfma_f32_32x32x16_f16 a[0:15], v[24:27], v[52:55], 0
	ds_read_b128 v[24:27], v84 offset:17408
	v_mfma_f32_32x32x16_f16 a[80:95], v[28:31], v[56:59], a[80:95]
	s_add_u32 m0, s46, 0x0
	s_add_u32 s40, s40, 0x1800
	s_addc_u32 s41, s41, 0
	global_load_lds_dwordx4 v84, s[40:41]
	v_mfma_f32_32x32x16_f16 a[64:79], v[32:35], v[56:59], a[64:79]
	s_add_u32 m0, s47, 0x0
	s_add_u32 s42, s42, 0x1800
	s_addc_u32 s43, s43, 0
	global_load_lds_dwordx4 v84, s[42:43]
	v_mfma_f32_32x32x16_f16 a[48:63], v[36:39], v[56:59], a[48:63]
	s_add_u32 m0, s48, 0x0
	s_add_u32 s44, s44, 0x1800
	s_addc_u32 s45, s45, 0
	global_load_lds_dwordx4 v84, s[44:45]
	v_mfma_f32_32x32x16_f16 a[32:47], v[40:43], v[56:59], a[32:47]
	v_mfma_f32_32x32x16_f16 a[16:31], v[44:47], v[56:59], a[16:31]
	v_mfma_f32_32x32x16_f16 a[0:15], v[48:51], v[56:59], a[0:15]
	ds_read_b128 v[28:31], v84 offset:18432
	ds_read_b128 v[32:35], v84 offset:19456
	ds_read_b128 v[36:39], v84 offset:20480
	ds_read_b128 v[40:43], v84 offset:21504
	ds_read_b128 v[44:47], v84 offset:22528
	ds_read_b128 v[48:51], v84 offset:23552
	s_waitcnt lgkmcnt(6)
	v_mfma_f32_32x32x16_f16 a[80:95], v[4:7], v[60:63], a[80:95]
	s_waitcnt vmcnt(23)
	ds_write_b128 v81, v[132:135]
	ds_write_b128 v81, v[136:139] offset:1024
	ds_write_b128 v81, v[140:143] offset:2048
	ds_write_b128 v81, v[144:147] offset:3072
	v_mfma_f32_32x32x16_f16 a[64:79], v[8:11], v[60:63], a[64:79]
	ds_read_b128 v[100:103], v95
	ds_read_b128 v[104:107], v96
	ds_read_b128 v[108:111], v97
	ds_read_b128 v[112:115], v94
	v_mfma_f32_32x32x16_f16 a[48:63], v[12:15], v[60:63], a[48:63]
	global_load_dwordx4 v[132:135], v64, s[4:5] offset:512
	global_load_dwordx4 v[136:139], v66, s[4:5] offset:512
	global_load_dwordx4 v[140:143], v68, s[4:5] offset:512
	global_load_dwordx4 v[144:147], v70, s[4:5] offset:512
	s_waitcnt vmcnt(14)
	s_waitcnt lgkmcnt(8)
	s_barrier
	ds_read_b128 v[4:7], v84 offset:54208
	ds_read_b128 v[8:11], v84 offset:55232
	ds_read_b128 v[12:15], v84 offset:56256
	v_mfma_f32_32x32x16_f16 a[32:47], v[16:19], v[60:63], a[32:47]
	ds_read_b128 v[16:19], v84 offset:57280
	v_mfma_f32_32x32x16_f16 a[16:31], v[20:23], v[60:63], a[16:31]
	ds_read_b128 v[20:23], v84 offset:58304
	v_mfma_f32_32x32x16_f16 a[0:15], v[24:27], v[60:63], a[0:15]
	ds_read_b128 v[24:27], v84 offset:59328
	v_mfma_f32_32x32x16_f16 a[80:95], v[28:31], v[0:3], a[80:95]
	s_add_u32 m0, s46, 0x3000
	s_add_u32 s40, s40, 0x1800
	s_addc_u32 s41, s41, 0
	global_load_lds_dwordx4 v84, s[40:41]
	v_mfma_f32_32x32x16_f16 a[64:79], v[32:35], v[0:3], a[64:79]
	s_add_u32 m0, s47, 0x3000
	s_add_u32 s42, s42, 0x1800
	s_addc_u32 s43, s43, 0
	global_load_lds_dwordx4 v84, s[42:43]
	v_mfma_f32_32x32x16_f16 a[48:63], v[36:39], v[0:3], a[48:63]
	s_add_u32 m0, s48, 0x3000
	s_add_u32 s44, s44, 0x1800
	s_addc_u32 s45, s45, 0
	global_load_lds_dwordx4 v84, s[44:45]
	v_mfma_f32_32x32x16_f16 a[32:47], v[40:43], v[0:3], a[32:47]
	v_mfma_f32_32x32x16_f16 a[16:31], v[44:47], v[0:3], a[16:31]
	v_mfma_f32_32x32x16_f16 a[0:15], v[48:51], v[0:3], a[0:15]
	s_waitcnt lgkmcnt(6)
	ds_read_b128 v[28:31], v84 offset:60352
	ds_read_b128 v[32:35], v84 offset:61376
	ds_read_b128 v[36:39], v84 offset:62400
	ds_read_b128 v[40:43], v84 offset:63424
	ds_read_b128 v[44:47], v84 offset:64448
	ds_read_b128 v[48:51], v84 offset:65472
	s_waitcnt lgkmcnt(6)
	v_mfma_f32_32x32x16_f16 a[80:95], v[4:7], v[100:103], a[80:95]
	v_mfma_f32_32x32x16_f16 a[64:79], v[8:11], v[100:103], a[64:79]
	v_mfma_f32_32x32x16_f16 a[48:63], v[12:15], v[100:103], a[48:63]
	s_waitcnt vmcnt(14)
	s_waitcnt lgkmcnt(0)
	s_barrier
	ds_read_b128 v[4:7], v98
	ds_read_b128 v[8:11], v98 offset:1024
	ds_read_b128 v[12:15], v98 offset:2048
	v_mfma_f32_32x32x16_f16 a[32:47], v[16:19], v[100:103], a[32:47]
	ds_read_b128 v[16:19], v98 offset:3072
	v_mfma_f32_32x32x16_f16 a[16:31], v[20:23], v[100:103], a[16:31]
	ds_read_b128 v[20:23], v98 offset:4096
	v_mfma_f32_32x32x16_f16 a[0:15], v[24:27], v[100:103], a[0:15]
	ds_read_b128 v[24:27], v98 offset:5120
	v_mfma_f32_32x32x16_f16 a[80:95], v[28:31], v[104:107], a[80:95]
	s_add_u32 m0, s46, 0xd3c0
	s_add_u32 s40, s40, 0x1800
	s_addc_u32 s41, s41, 0
	global_load_lds_dwordx4 v84, s[40:41]
	v_mfma_f32_32x32x16_f16 a[64:79], v[32:35], v[104:107], a[64:79]
	s_add_u32 m0, s47, 0xd3c0
	s_add_u32 s42, s42, 0x1800
	s_addc_u32 s43, s43, 0
	global_load_lds_dwordx4 v84, s[42:43]
	v_mfma_f32_32x32x16_f16 a[48:63], v[36:39], v[104:107], a[48:63]
	s_add_u32 m0, s48, 0xd3c0
	s_add_u32 s44, s44, 0x1800
	s_addc_u32 s45, s45, 0
	global_load_lds_dwordx4 v84, s[44:45]
	v_mfma_f32_32x32x16_f16 a[32:47], v[40:43], v[104:107], a[32:47]
	v_mfma_f32_32x32x16_f16 a[16:31], v[44:47], v[104:107], a[16:31]
	v_mfma_f32_32x32x16_f16 a[0:15], v[48:51], v[104:107], a[0:15]
	ds_read_b128 v[28:31], v98 offset:6144
	ds_read_b128 v[32:35], v98 offset:7168
	ds_read_b128 v[36:39], v98 offset:8192
	ds_read_b128 v[40:43], v98 offset:9216
	ds_read_b128 v[44:47], v98 offset:10240
	ds_read_b128 v[48:51], v98 offset:11264
	s_waitcnt lgkmcnt(6)
	v_mfma_f32_32x32x16_f16 a[80:95], v[4:7], v[108:111], a[80:95]
	s_waitcnt vmcnt(29)
	ds_write_b128 v81, v[148:151]
	ds_write_b128 v81, v[152:155] offset:1024
	ds_write_b128 v81, v[156:159] offset:2048
	ds_write_b128 v81, v[72:75] offset:3072
	v_mfma_f32_32x32x16_f16 a[64:79], v[8:11], v[108:111], a[64:79]
	ds_read_b128 v[52:55], v95
	ds_read_b128 v[56:59], v96
	ds_read_b128 v[60:63], v97
	ds_read_b128 v[0:3], v94
	v_mfma_f32_32x32x16_f16 a[48:63], v[12:15], v[108:111], a[48:63]
	global_load_dwordx4 v[148:151], v64, s[4:5] offset:640
	global_load_dwordx4 v[152:155], v66, s[4:5] offset:640
	global_load_dwordx4 v[156:159], v68, s[4:5] offset:640
	global_load_dwordx4 v[72:75], v70, s[4:5] offset:640
	s_waitcnt vmcnt(14)
	s_waitcnt lgkmcnt(8)
	s_barrier
	ds_read_b128 v[4:7], v84 offset:0
	ds_read_b128 v[8:11], v84 offset:1024
	ds_read_b128 v[12:15], v84 offset:2048
	v_mfma_f32_32x32x16_f16 a[32:47], v[16:19], v[108:111], a[32:47]
	ds_read_b128 v[16:19], v84 offset:3072
	v_mfma_f32_32x32x16_f16 a[16:31], v[20:23], v[108:111], a[16:31]
	ds_read_b128 v[20:23], v84 offset:4096
	v_mfma_f32_32x32x16_f16 a[0:15], v[24:27], v[108:111], a[0:15]
	ds_read_b128 v[24:27], v84 offset:5120
	v_mfma_f32_32x32x16_f16 a[80:95], v[28:31], v[112:115], a[80:95]
	s_add_u32 m0, s46, 0x103c0
	s_add_u32 s40, s40, 0x1800
	s_addc_u32 s41, s41, 0
	global_load_lds_dwordx4 v84, s[40:41]
	v_mfma_f32_32x32x16_f16 a[64:79], v[32:35], v[112:115], a[64:79]
	s_add_u32 m0, s47, 0x103c0
	s_add_u32 s42, s42, 0x1800
	s_addc_u32 s43, s43, 0
	global_load_lds_dwordx4 v84, s[42:43]
	v_mfma_f32_32x32x16_f16 a[48:63], v[36:39], v[112:115], a[48:63]
	s_add_u32 m0, s48, 0x103c0
	s_add_u32 s44, s44, 0x1800
	s_addc_u32 s45, s45, 0
	global_load_lds_dwordx4 v84, s[44:45]
	v_mfma_f32_32x32x16_f16 a[32:47], v[40:43], v[112:115], a[32:47]
	v_mfma_f32_32x32x16_f16 a[16:31], v[44:47], v[112:115], a[16:31]
	v_mfma_f32_32x32x16_f16 a[0:15], v[48:51], v[112:115], a[0:15]
	s_waitcnt lgkmcnt(6)
	ds_read_b128 v[28:31], v84 offset:6144
	ds_read_b128 v[32:35], v84 offset:7168
	ds_read_b128 v[36:39], v84 offset:8192
	ds_read_b128 v[40:43], v84 offset:9216
	ds_read_b128 v[44:47], v84 offset:10240
	ds_read_b128 v[48:51], v84 offset:11264
	s_waitcnt lgkmcnt(6)
	v_mfma_f32_32x32x16_f16 a[80:95], v[4:7], v[52:55], a[80:95]
	v_mfma_f32_32x32x16_f16 a[64:79], v[8:11], v[52:55], a[64:79]
	v_mfma_f32_32x32x16_f16 a[48:63], v[12:15], v[52:55], a[48:63]
	s_waitcnt vmcnt(10)
	s_waitcnt lgkmcnt(0)
	s_barrier
	ds_read_b128 v[4:7], v84 offset:12288
	ds_read_b128 v[8:11], v84 offset:13312
	ds_read_b128 v[12:15], v84 offset:14336
	v_mfma_f32_32x32x16_f16 a[32:47], v[16:19], v[52:55], a[32:47]
	ds_read_b128 v[16:19], v84 offset:15360
	v_mfma_f32_32x32x16_f16 a[16:31], v[20:23], v[52:55], a[16:31]
	ds_read_b128 v[20:23], v84 offset:16384
	v_mfma_f32_32x32x16_f16 a[0:15], v[24:27], v[52:55], a[0:15]
	ds_read_b128 v[24:27], v84 offset:17408
	v_mfma_f32_32x32x16_f16 a[80:95], v[28:31], v[56:59], a[80:95]
	s_add_u32 m0, s46, 0x0
	s_add_u32 s40, s40, 0x1800
	s_addc_u32 s41, s41, 0
	global_load_lds_dwordx4 v84, s[40:41]
	v_mfma_f32_32x32x16_f16 a[64:79], v[32:35], v[56:59], a[64:79]
	s_add_u32 m0, s47, 0x0
	s_add_u32 s42, s42, 0x1800
	s_addc_u32 s43, s43, 0
	global_load_lds_dwordx4 v84, s[42:43]
	v_mfma_f32_32x32x16_f16 a[48:63], v[36:39], v[56:59], a[48:63]
	s_add_u32 m0, s48, 0x0
	s_add_u32 s44, s44, 0x1800
	s_addc_u32 s45, s45, 0
	global_load_lds_dwordx4 v84, s[44:45]
	v_mfma_f32_32x32x16_f16 a[32:47], v[40:43], v[56:59], a[32:47]
	v_mfma_f32_32x32x16_f16 a[16:31], v[44:47], v[56:59], a[16:31]
	v_mfma_f32_32x32x16_f16 a[0:15], v[48:51], v[56:59], a[0:15]
	ds_read_b128 v[28:31], v84 offset:18432
	ds_read_b128 v[32:35], v84 offset:19456
	ds_read_b128 v[36:39], v84 offset:20480
	ds_read_b128 v[40:43], v84 offset:21504
	ds_read_b128 v[44:47], v84 offset:22528
	ds_read_b128 v[48:51], v84 offset:23552
	s_waitcnt lgkmcnt(6)
	v_mfma_f32_32x32x16_f16 a[80:95], v[4:7], v[60:63], a[80:95]
	s_waitcnt vmcnt(23)
	ds_write_b128 v81, v[116:119]
	ds_write_b128 v81, v[120:123] offset:1024
	ds_write_b128 v81, v[124:127] offset:2048
	ds_write_b128 v81, v[128:131] offset:3072
	v_mfma_f32_32x32x16_f16 a[64:79], v[8:11], v[60:63], a[64:79]
	ds_read_b128 v[100:103], v95
	ds_read_b128 v[104:107], v96
	ds_read_b128 v[108:111], v97
	ds_read_b128 v[112:115], v94
	v_mfma_f32_32x32x16_f16 a[48:63], v[12:15], v[60:63], a[48:63]
	global_load_dwordx4 v[116:119], v64, s[4:5] offset:768
	global_load_dwordx4 v[120:123], v66, s[4:5] offset:768
	global_load_dwordx4 v[124:127], v68, s[4:5] offset:768
	global_load_dwordx4 v[128:131], v70, s[4:5] offset:768
	s_waitcnt vmcnt(14)
	s_waitcnt lgkmcnt(8)
	s_barrier
	ds_read_b128 v[4:7], v84 offset:54208
	ds_read_b128 v[8:11], v84 offset:55232
	ds_read_b128 v[12:15], v84 offset:56256
	v_mfma_f32_32x32x16_f16 a[32:47], v[16:19], v[60:63], a[32:47]
	ds_read_b128 v[16:19], v84 offset:57280
	v_mfma_f32_32x32x16_f16 a[16:31], v[20:23], v[60:63], a[16:31]
	ds_read_b128 v[20:23], v84 offset:58304
	v_mfma_f32_32x32x16_f16 a[0:15], v[24:27], v[60:63], a[0:15]
	ds_read_b128 v[24:27], v84 offset:59328
	v_mfma_f32_32x32x16_f16 a[80:95], v[28:31], v[0:3], a[80:95]
	s_add_u32 m0, s46, 0x3000
	s_add_u32 s40, s40, 0x1800
	s_addc_u32 s41, s41, 0
	global_load_lds_dwordx4 v84, s[40:41]
	v_mfma_f32_32x32x16_f16 a[64:79], v[32:35], v[0:3], a[64:79]
	s_add_u32 m0, s47, 0x3000
	s_add_u32 s42, s42, 0x1800
	s_addc_u32 s43, s43, 0
	global_load_lds_dwordx4 v84, s[42:43]
	v_mfma_f32_32x32x16_f16 a[48:63], v[36:39], v[0:3], a[48:63]
	s_add_u32 m0, s48, 0x3000
	s_add_u32 s44, s44, 0x1800
	s_addc_u32 s45, s45, 0
	global_load_lds_dwordx4 v84, s[44:45]
	v_mfma_f32_32x32x16_f16 a[32:47], v[40:43], v[0:3], a[32:47]
	v_mfma_f32_32x32x16_f16 a[16:31], v[44:47], v[0:3], a[16:31]
	v_mfma_f32_32x32x16_f16 a[0:15], v[48:51], v[0:3], a[0:15]
	s_waitcnt lgkmcnt(6)
	ds_read_b128 v[28:31], v84 offset:60352
	ds_read_b128 v[32:35], v84 offset:61376
	ds_read_b128 v[36:39], v84 offset:62400
	ds_read_b128 v[40:43], v84 offset:63424
	ds_read_b128 v[44:47], v84 offset:64448
	ds_read_b128 v[48:51], v84 offset:65472
	s_waitcnt lgkmcnt(6)
	v_mfma_f32_32x32x16_f16 a[80:95], v[4:7], v[100:103], a[80:95]
	v_mfma_f32_32x32x16_f16 a[64:79], v[8:11], v[100:103], a[64:79]
	v_mfma_f32_32x32x16_f16 a[48:63], v[12:15], v[100:103], a[48:63]
	s_waitcnt vmcnt(10)
	s_waitcnt lgkmcnt(0)
	s_barrier
	ds_read_b128 v[4:7], v98
	ds_read_b128 v[8:11], v98 offset:1024
	ds_read_b128 v[12:15], v98 offset:2048
	v_mfma_f32_32x32x16_f16 a[32:47], v[16:19], v[100:103], a[32:47]
	ds_read_b128 v[16:19], v98 offset:3072
	v_mfma_f32_32x32x16_f16 a[16:31], v[20:23], v[100:103], a[16:31]
	ds_read_b128 v[20:23], v98 offset:4096
	v_mfma_f32_32x32x16_f16 a[0:15], v[24:27], v[100:103], a[0:15]
	ds_read_b128 v[24:27], v98 offset:5120
	v_mfma_f32_32x32x16_f16 a[80:95], v[28:31], v[104:107], a[80:95]
	s_add_u32 m0, s46, 0xd3c0
	s_add_u32 s40, s40, 0x1800
	s_addc_u32 s41, s41, 0
	global_load_lds_dwordx4 v84, s[40:41]
	v_mfma_f32_32x32x16_f16 a[64:79], v[32:35], v[104:107], a[64:79]
	s_add_u32 m0, s47, 0xd3c0
	s_add_u32 s42, s42, 0x1800
	s_addc_u32 s43, s43, 0
	global_load_lds_dwordx4 v84, s[42:43]
	v_mfma_f32_32x32x16_f16 a[48:63], v[36:39], v[104:107], a[48:63]
	s_add_u32 m0, s48, 0xd3c0
	s_add_u32 s44, s44, 0x1800
	s_addc_u32 s45, s45, 0
	global_load_lds_dwordx4 v84, s[44:45]
	v_mfma_f32_32x32x16_f16 a[32:47], v[40:43], v[104:107], a[32:47]
	v_mfma_f32_32x32x16_f16 a[16:31], v[44:47], v[104:107], a[16:31]
	v_mfma_f32_32x32x16_f16 a[0:15], v[48:51], v[104:107], a[0:15]
	ds_read_b128 v[28:31], v98 offset:6144
	ds_read_b128 v[32:35], v98 offset:7168
	ds_read_b128 v[36:39], v98 offset:8192
	ds_read_b128 v[40:43], v98 offset:9216
	ds_read_b128 v[44:47], v98 offset:10240
	ds_read_b128 v[48:51], v98 offset:11264
	s_waitcnt lgkmcnt(6)
	v_mfma_f32_32x32x16_f16 a[80:95], v[4:7], v[108:111], a[80:95]
	s_waitcnt vmcnt(26)
	ds_write_b128 v81, v[132:135]
	ds_write_b128 v81, v[136:139] offset:1024
	ds_write_b128 v81, v[140:143] offset:2048
	ds_write_b128 v81, v[144:147] offset:3072
	v_mfma_f32_32x32x16_f16 a[64:79], v[8:11], v[108:111], a[64:79]
	ds_read_b128 v[52:55], v95
	ds_read_b128 v[56:59], v96
	ds_read_b128 v[60:63], v97
	ds_read_b128 v[0:3], v94
	v_mfma_f32_32x32x16_f16 a[48:63], v[12:15], v[108:111], a[48:63]
	global_load_dwordx4 v[132:135], v64, s[4:5] offset:896
	global_load_dwordx4 v[136:139], v66, s[4:5] offset:896
	global_load_dwordx4 v[140:143], v68, s[4:5] offset:896
	global_load_dwordx4 v[144:147], v70, s[4:5] offset:896
	s_waitcnt vmcnt(14)
	s_waitcnt lgkmcnt(8)
	s_barrier
	ds_read_b128 v[4:7], v84 offset:0
	ds_read_b128 v[8:11], v84 offset:1024
	ds_read_b128 v[12:15], v84 offset:2048
	v_mfma_f32_32x32x16_f16 a[32:47], v[16:19], v[108:111], a[32:47]
	ds_read_b128 v[16:19], v84 offset:3072
	v_mfma_f32_32x32x16_f16 a[16:31], v[20:23], v[108:111], a[16:31]
	ds_read_b128 v[20:23], v84 offset:4096
	v_mfma_f32_32x32x16_f16 a[0:15], v[24:27], v[108:111], a[0:15]
	ds_read_b128 v[24:27], v84 offset:5120
	v_mfma_f32_32x32x16_f16 a[80:95], v[28:31], v[112:115], a[80:95]
	s_add_u32 m0, s46, 0x103c0
	s_add_u32 s40, s40, 0x1800
	s_addc_u32 s41, s41, 0
	global_load_lds_dwordx4 v84, s[40:41]
	v_mfma_f32_32x32x16_f16 a[64:79], v[32:35], v[112:115], a[64:79]
	s_add_u32 m0, s47, 0x103c0
	s_add_u32 s42, s42, 0x1800
	s_addc_u32 s43, s43, 0
	global_load_lds_dwordx4 v84, s[42:43]
	v_mfma_f32_32x32x16_f16 a[48:63], v[36:39], v[112:115], a[48:63]
	s_add_u32 m0, s48, 0x103c0
	s_add_u32 s44, s44, 0x1800
	s_addc_u32 s45, s45, 0
	global_load_lds_dwordx4 v84, s[44:45]
	v_mfma_f32_32x32x16_f16 a[32:47], v[40:43], v[112:115], a[32:47]
	v_mfma_f32_32x32x16_f16 a[16:31], v[44:47], v[112:115], a[16:31]
	v_mfma_f32_32x32x16_f16 a[0:15], v[48:51], v[112:115], a[0:15]
	s_waitcnt lgkmcnt(6)
	ds_read_b128 v[28:31], v84 offset:6144
	ds_read_b128 v[32:35], v84 offset:7168
	ds_read_b128 v[36:39], v84 offset:8192
	ds_read_b128 v[40:43], v84 offset:9216
	ds_read_b128 v[44:47], v84 offset:10240
	ds_read_b128 v[48:51], v84 offset:11264
	s_waitcnt lgkmcnt(6)
	v_mfma_f32_32x32x16_f16 a[80:95], v[4:7], v[52:55], a[80:95]
	v_mfma_f32_32x32x16_f16 a[64:79], v[8:11], v[52:55], a[64:79]
	v_mfma_f32_32x32x16_f16 a[48:63], v[12:15], v[52:55], a[48:63]
	s_waitcnt vmcnt(10)
	s_waitcnt lgkmcnt(0)
	s_barrier
	ds_read_b128 v[4:7], v84 offset:12288
	ds_read_b128 v[8:11], v84 offset:13312
	ds_read_b128 v[12:15], v84 offset:14336
	v_mfma_f32_32x32x16_f16 a[32:47], v[16:19], v[52:55], a[32:47]
	ds_read_b128 v[16:19], v84 offset:15360
	v_mfma_f32_32x32x16_f16 a[16:31], v[20:23], v[52:55], a[16:31]
	ds_read_b128 v[20:23], v84 offset:16384
	v_mfma_f32_32x32x16_f16 a[0:15], v[24:27], v[52:55], a[0:15]
	ds_read_b128 v[24:27], v84 offset:17408
	v_mfma_f32_32x32x16_f16 a[80:95], v[28:31], v[56:59], a[80:95]
	s_add_u32 m0, s46, 0x0
	s_add_u32 s40, s40, 0x1800
	s_addc_u32 s41, s41, 0
	global_load_lds_dwordx4 v84, s[40:41]
	v_mfma_f32_32x32x16_f16 a[64:79], v[32:35], v[56:59], a[64:79]
	s_add_u32 m0, s47, 0x0
	s_add_u32 s42, s42, 0x1800
	s_addc_u32 s43, s43, 0
	global_load_lds_dwordx4 v84, s[42:43]
	v_mfma_f32_32x32x16_f16 a[48:63], v[36:39], v[56:59], a[48:63]
	s_add_u32 m0, s48, 0x0
	s_add_u32 s44, s44, 0x1800
	s_addc_u32 s45, s45, 0
	global_load_lds_dwordx4 v84, s[44:45]
	v_mfma_f32_32x32x16_f16 a[32:47], v[40:43], v[56:59], a[32:47]
	v_mfma_f32_32x32x16_f16 a[16:31], v[44:47], v[56:59], a[16:31]
	v_mfma_f32_32x32x16_f16 a[0:15], v[48:51], v[56:59], a[0:15]
	ds_read_b128 v[28:31], v84 offset:18432
	ds_read_b128 v[32:35], v84 offset:19456
	ds_read_b128 v[36:39], v84 offset:20480
	ds_read_b128 v[40:43], v84 offset:21504
	ds_read_b128 v[44:47], v84 offset:22528
	ds_read_b128 v[48:51], v84 offset:23552
	s_waitcnt lgkmcnt(6)
	v_mfma_f32_32x32x16_f16 a[80:95], v[4:7], v[60:63], a[80:95]
	s_waitcnt vmcnt(26)
	ds_write_b128 v81, v[148:151]
	ds_write_b128 v81, v[152:155] offset:1024
	ds_write_b128 v81, v[156:159] offset:2048
	ds_write_b128 v81, v[72:75] offset:3072
	v_mfma_f32_32x32x16_f16 a[64:79], v[8:11], v[60:63], a[64:79]
	ds_read_b128 v[100:103], v95
	ds_read_b128 v[104:107], v96
	ds_read_b128 v[108:111], v97
	ds_read_b128 v[112:115], v94
	v_mfma_f32_32x32x16_f16 a[48:63], v[12:15], v[60:63], a[48:63]
	global_load_dwordx4 v[148:151], v64, s[4:5] offset:1024
	global_load_dwordx4 v[152:155], v66, s[4:5] offset:1024
	global_load_dwordx4 v[156:159], v68, s[4:5] offset:1024
	global_load_dwordx4 v[72:75], v70, s[4:5] offset:1024
	s_waitcnt vmcnt(14)
	s_waitcnt lgkmcnt(8)
	s_barrier
	ds_read_b128 v[4:7], v84 offset:54208
	ds_read_b128 v[8:11], v84 offset:55232
	ds_read_b128 v[12:15], v84 offset:56256
	v_mfma_f32_32x32x16_f16 a[32:47], v[16:19], v[60:63], a[32:47]
	ds_read_b128 v[16:19], v84 offset:57280
	v_mfma_f32_32x32x16_f16 a[16:31], v[20:23], v[60:63], a[16:31]
	ds_read_b128 v[20:23], v84 offset:58304
	v_mfma_f32_32x32x16_f16 a[0:15], v[24:27], v[60:63], a[0:15]
	ds_read_b128 v[24:27], v84 offset:59328
	v_mfma_f32_32x32x16_f16 a[80:95], v[28:31], v[0:3], a[80:95]
	s_add_u32 m0, s46, 0x3000
	s_add_u32 s40, s40, 0x1800
	s_addc_u32 s41, s41, 0
	global_load_lds_dwordx4 v84, s[40:41]
	v_mfma_f32_32x32x16_f16 a[64:79], v[32:35], v[0:3], a[64:79]
	s_add_u32 m0, s47, 0x3000
	s_add_u32 s42, s42, 0x1800
	s_addc_u32 s43, s43, 0
	global_load_lds_dwordx4 v84, s[42:43]
	v_mfma_f32_32x32x16_f16 a[48:63], v[36:39], v[0:3], a[48:63]
	s_add_u32 m0, s48, 0x3000
	s_add_u32 s44, s44, 0x1800
	s_addc_u32 s45, s45, 0
	global_load_lds_dwordx4 v84, s[44:45]
	v_mfma_f32_32x32x16_f16 a[32:47], v[40:43], v[0:3], a[32:47]
	v_mfma_f32_32x32x16_f16 a[16:31], v[44:47], v[0:3], a[16:31]
	v_mfma_f32_32x32x16_f16 a[0:15], v[48:51], v[0:3], a[0:15]
	s_waitcnt lgkmcnt(6)
	ds_read_b128 v[28:31], v84 offset:60352
	ds_read_b128 v[32:35], v84 offset:61376
	ds_read_b128 v[36:39], v84 offset:62400
	ds_read_b128 v[40:43], v84 offset:63424
	ds_read_b128 v[44:47], v84 offset:64448
	ds_read_b128 v[48:51], v84 offset:65472
	s_waitcnt lgkmcnt(6)
	v_mfma_f32_32x32x16_f16 a[80:95], v[4:7], v[100:103], a[80:95]
	v_mfma_f32_32x32x16_f16 a[64:79], v[8:11], v[100:103], a[64:79]
	v_mfma_f32_32x32x16_f16 a[48:63], v[12:15], v[100:103], a[48:63]
	s_waitcnt vmcnt(10)
	s_waitcnt lgkmcnt(0)
	s_barrier
	ds_read_b128 v[4:7], v98
	ds_read_b128 v[8:11], v98 offset:1024
	ds_read_b128 v[12:15], v98 offset:2048
	v_mfma_f32_32x32x16_f16 a[32:47], v[16:19], v[100:103], a[32:47]
	ds_read_b128 v[16:19], v98 offset:3072
	v_mfma_f32_32x32x16_f16 a[16:31], v[20:23], v[100:103], a[16:31]
	ds_read_b128 v[20:23], v98 offset:4096
	v_mfma_f32_32x32x16_f16 a[0:15], v[24:27], v[100:103], a[0:15]
	ds_read_b128 v[24:27], v98 offset:5120
	v_mfma_f32_32x32x16_f16 a[80:95], v[28:31], v[104:107], a[80:95]
	s_add_u32 m0, s46, 0xd3c0
	s_add_u32 s40, s40, 0x1800
	s_addc_u32 s41, s41, 0
	global_load_lds_dwordx4 v84, s[40:41]
	v_mfma_f32_32x32x16_f16 a[64:79], v[32:35], v[104:107], a[64:79]
	s_add_u32 m0, s47, 0xd3c0
	s_add_u32 s42, s42, 0x1800
	s_addc_u32 s43, s43, 0
	global_load_lds_dwordx4 v84, s[42:43]
	v_mfma_f32_32x32x16_f16 a[48:63], v[36:39], v[104:107], a[48:63]
	s_add_u32 m0, s48, 0xd3c0
	s_add_u32 s44, s44, 0x1800
	s_addc_u32 s45, s45, 0
	global_load_lds_dwordx4 v84, s[44:45]
	v_mfma_f32_32x32x16_f16 a[32:47], v[40:43], v[104:107], a[32:47]
	v_mfma_f32_32x32x16_f16 a[16:31], v[44:47], v[104:107], a[16:31]
	v_mfma_f32_32x32x16_f16 a[0:15], v[48:51], v[104:107], a[0:15]
	ds_read_b128 v[28:31], v98 offset:6144
	ds_read_b128 v[32:35], v98 offset:7168
	ds_read_b128 v[36:39], v98 offset:8192
	ds_read_b128 v[40:43], v98 offset:9216
	ds_read_b128 v[44:47], v98 offset:10240
	ds_read_b128 v[48:51], v98 offset:11264
	s_waitcnt lgkmcnt(6)
	v_mfma_f32_32x32x16_f16 a[80:95], v[4:7], v[108:111], a[80:95]
	s_waitcnt vmcnt(26)
	ds_write_b128 v81, v[116:119]
	ds_write_b128 v81, v[120:123] offset:1024
	ds_write_b128 v81, v[124:127] offset:2048
	ds_write_b128 v81, v[128:131] offset:3072
	v_mfma_f32_32x32x16_f16 a[64:79], v[8:11], v[108:111], a[64:79]
	ds_read_b128 v[52:55], v95
	ds_read_b128 v[56:59], v96
	ds_read_b128 v[60:63], v97
	ds_read_b128 v[0:3], v94
	v_mfma_f32_32x32x16_f16 a[48:63], v[12:15], v[108:111], a[48:63]
	global_load_dwordx4 v[116:119], v64, s[4:5] offset:1152
	global_load_dwordx4 v[120:123], v66, s[4:5] offset:1152
	global_load_dwordx4 v[124:127], v68, s[4:5] offset:1152
	global_load_dwordx4 v[128:131], v70, s[4:5] offset:1152
	s_waitcnt vmcnt(14)
	s_waitcnt lgkmcnt(8)
	s_barrier
	ds_read_b128 v[4:7], v84 offset:0
	ds_read_b128 v[8:11], v84 offset:1024
	ds_read_b128 v[12:15], v84 offset:2048
	v_mfma_f32_32x32x16_f16 a[32:47], v[16:19], v[108:111], a[32:47]
	ds_read_b128 v[16:19], v84 offset:3072
	v_mfma_f32_32x32x16_f16 a[16:31], v[20:23], v[108:111], a[16:31]
	ds_read_b128 v[20:23], v84 offset:4096
	v_mfma_f32_32x32x16_f16 a[0:15], v[24:27], v[108:111], a[0:15]
	ds_read_b128 v[24:27], v84 offset:5120
	v_mfma_f32_32x32x16_f16 a[80:95], v[28:31], v[112:115], a[80:95]
	s_add_u32 m0, s46, 0x103c0
	s_add_u32 s40, s40, 0x1800
	s_addc_u32 s41, s41, 0
	global_load_lds_dwordx4 v84, s[40:41]
	v_mfma_f32_32x32x16_f16 a[64:79], v[32:35], v[112:115], a[64:79]
	s_add_u32 m0, s47, 0x103c0
	s_add_u32 s42, s42, 0x1800
	s_addc_u32 s43, s43, 0
	global_load_lds_dwordx4 v84, s[42:43]
	v_mfma_f32_32x32x16_f16 a[48:63], v[36:39], v[112:115], a[48:63]
	s_add_u32 m0, s48, 0x103c0
	s_add_u32 s44, s44, 0x1800
	s_addc_u32 s45, s45, 0
	global_load_lds_dwordx4 v84, s[44:45]
	v_mfma_f32_32x32x16_f16 a[32:47], v[40:43], v[112:115], a[32:47]
	v_mfma_f32_32x32x16_f16 a[16:31], v[44:47], v[112:115], a[16:31]
	v_mfma_f32_32x32x16_f16 a[0:15], v[48:51], v[112:115], a[0:15]
	s_waitcnt lgkmcnt(6)
	ds_read_b128 v[28:31], v84 offset:6144
	ds_read_b128 v[32:35], v84 offset:7168
	ds_read_b128 v[36:39], v84 offset:8192
	ds_read_b128 v[40:43], v84 offset:9216
	ds_read_b128 v[44:47], v84 offset:10240
	ds_read_b128 v[48:51], v84 offset:11264
	s_waitcnt lgkmcnt(6)
	v_mfma_f32_32x32x16_f16 a[80:95], v[4:7], v[52:55], a[80:95]
	v_mfma_f32_32x32x16_f16 a[64:79], v[8:11], v[52:55], a[64:79]
	v_mfma_f32_32x32x16_f16 a[48:63], v[12:15], v[52:55], a[48:63]
	s_waitcnt vmcnt(10)
	s_waitcnt lgkmcnt(0)
	s_barrier
	ds_read_b128 v[4:7], v84 offset:12288
	ds_read_b128 v[8:11], v84 offset:13312
	ds_read_b128 v[12:15], v84 offset:14336
	v_mfma_f32_32x32x16_f16 a[32:47], v[16:19], v[52:55], a[32:47]
	ds_read_b128 v[16:19], v84 offset:15360
	v_mfma_f32_32x32x16_f16 a[16:31], v[20:23], v[52:55], a[16:31]
	ds_read_b128 v[20:23], v84 offset:16384
	v_mfma_f32_32x32x16_f16 a[0:15], v[24:27], v[52:55], a[0:15]
	ds_read_b128 v[24:27], v84 offset:17408
	v_mfma_f32_32x32x16_f16 a[80:95], v[28:31], v[56:59], a[80:95]
	s_add_u32 m0, s46, 0x0
	s_add_u32 s40, s40, 0x1800
	s_addc_u32 s41, s41, 0
	global_load_lds_dwordx4 v84, s[40:41]
	v_mfma_f32_32x32x16_f16 a[64:79], v[32:35], v[56:59], a[64:79]
	s_add_u32 m0, s47, 0x0
	s_add_u32 s42, s42, 0x1800
	s_addc_u32 s43, s43, 0
	global_load_lds_dwordx4 v84, s[42:43]
	v_mfma_f32_32x32x16_f16 a[48:63], v[36:39], v[56:59], a[48:63]
	s_add_u32 m0, s48, 0x0
	s_add_u32 s44, s44, 0x1800
	s_addc_u32 s45, s45, 0
	global_load_lds_dwordx4 v84, s[44:45]
	v_mfma_f32_32x32x16_f16 a[32:47], v[40:43], v[56:59], a[32:47]
	v_mfma_f32_32x32x16_f16 a[16:31], v[44:47], v[56:59], a[16:31]
	v_mfma_f32_32x32x16_f16 a[0:15], v[48:51], v[56:59], a[0:15]
	ds_read_b128 v[28:31], v84 offset:18432
	ds_read_b128 v[32:35], v84 offset:19456
	ds_read_b128 v[36:39], v84 offset:20480
	ds_read_b128 v[40:43], v84 offset:21504
	ds_read_b128 v[44:47], v84 offset:22528
	ds_read_b128 v[48:51], v84 offset:23552
	s_waitcnt lgkmcnt(6)
	v_mfma_f32_32x32x16_f16 a[80:95], v[4:7], v[60:63], a[80:95]
	s_waitcnt vmcnt(26)
	ds_write_b128 v81, v[132:135]
	ds_write_b128 v81, v[136:139] offset:1024
	ds_write_b128 v81, v[140:143] offset:2048
	ds_write_b128 v81, v[144:147] offset:3072
	v_mfma_f32_32x32x16_f16 a[64:79], v[8:11], v[60:63], a[64:79]
	ds_read_b128 v[100:103], v95
	ds_read_b128 v[104:107], v96
	ds_read_b128 v[108:111], v97
	ds_read_b128 v[112:115], v94
	v_mfma_f32_32x32x16_f16 a[48:63], v[12:15], v[60:63], a[48:63]
	global_load_dwordx4 v[132:135], v64, s[4:5] offset:1280
	global_load_dwordx4 v[136:139], v66, s[4:5] offset:1280
	global_load_dwordx4 v[140:143], v68, s[4:5] offset:1280
	global_load_dwordx4 v[144:147], v70, s[4:5] offset:1280
	s_waitcnt vmcnt(14)
	s_waitcnt lgkmcnt(8)
	s_barrier
	ds_read_b128 v[4:7], v84 offset:54208
	ds_read_b128 v[8:11], v84 offset:55232
	ds_read_b128 v[12:15], v84 offset:56256
	v_mfma_f32_32x32x16_f16 a[32:47], v[16:19], v[60:63], a[32:47]
	ds_read_b128 v[16:19], v84 offset:57280
	v_mfma_f32_32x32x16_f16 a[16:31], v[20:23], v[60:63], a[16:31]
	ds_read_b128 v[20:23], v84 offset:58304
	v_mfma_f32_32x32x16_f16 a[0:15], v[24:27], v[60:63], a[0:15]
	ds_read_b128 v[24:27], v84 offset:59328
	v_mfma_f32_32x32x16_f16 a[80:95], v[28:31], v[0:3], a[80:95]
	s_add_u32 m0, s46, 0x3000
	s_add_u32 s40, s40, 0x1800
	s_addc_u32 s41, s41, 0
	global_load_lds_dwordx4 v84, s[40:41]
	v_mfma_f32_32x32x16_f16 a[64:79], v[32:35], v[0:3], a[64:79]
	s_add_u32 m0, s47, 0x3000
	s_add_u32 s42, s42, 0x1800
	s_addc_u32 s43, s43, 0
	global_load_lds_dwordx4 v84, s[42:43]
	v_mfma_f32_32x32x16_f16 a[48:63], v[36:39], v[0:3], a[48:63]
	s_add_u32 m0, s48, 0x3000
	s_add_u32 s44, s44, 0x1800
	s_addc_u32 s45, s45, 0
	global_load_lds_dwordx4 v84, s[44:45]
	v_mfma_f32_32x32x16_f16 a[32:47], v[40:43], v[0:3], a[32:47]
	v_mfma_f32_32x32x16_f16 a[16:31], v[44:47], v[0:3], a[16:31]
	v_mfma_f32_32x32x16_f16 a[0:15], v[48:51], v[0:3], a[0:15]
	s_waitcnt lgkmcnt(6)
	ds_read_b128 v[28:31], v84 offset:60352
	ds_read_b128 v[32:35], v84 offset:61376
	ds_read_b128 v[36:39], v84 offset:62400
	ds_read_b128 v[40:43], v84 offset:63424
	ds_read_b128 v[44:47], v84 offset:64448
	ds_read_b128 v[48:51], v84 offset:65472
	s_waitcnt lgkmcnt(6)
	v_mfma_f32_32x32x16_f16 a[80:95], v[4:7], v[100:103], a[80:95]
	v_mfma_f32_32x32x16_f16 a[64:79], v[8:11], v[100:103], a[64:79]
	v_mfma_f32_32x32x16_f16 a[48:63], v[12:15], v[100:103], a[48:63]
	s_waitcnt vmcnt(10)
	s_waitcnt lgkmcnt(0)
	s_barrier
	ds_read_b128 v[4:7], v98
	ds_read_b128 v[8:11], v98 offset:1024
	ds_read_b128 v[12:15], v98 offset:2048
	v_mfma_f32_32x32x16_f16 a[32:47], v[16:19], v[100:103], a[32:47]
	ds_read_b128 v[16:19], v98 offset:3072
	v_mfma_f32_32x32x16_f16 a[16:31], v[20:23], v[100:103], a[16:31]
	ds_read_b128 v[20:23], v98 offset:4096
	v_mfma_f32_32x32x16_f16 a[0:15], v[24:27], v[100:103], a[0:15]
	ds_read_b128 v[24:27], v98 offset:5120
	v_mfma_f32_32x32x16_f16 a[80:95], v[28:31], v[104:107], a[80:95]
	s_add_u32 m0, s46, 0xd3c0
	s_add_u32 s40, s40, 0x1800
	s_addc_u32 s41, s41, 0
	global_load_lds_dwordx4 v84, s[40:41]
	v_mfma_f32_32x32x16_f16 a[64:79], v[32:35], v[104:107], a[64:79]
	s_add_u32 m0, s47, 0xd3c0
	s_add_u32 s42, s42, 0x1800
	s_addc_u32 s43, s43, 0
	global_load_lds_dwordx4 v84, s[42:43]
	v_mfma_f32_32x32x16_f16 a[48:63], v[36:39], v[104:107], a[48:63]
	s_add_u32 m0, s48, 0xd3c0
	s_add_u32 s44, s44, 0x1800
	s_addc_u32 s45, s45, 0
	global_load_lds_dwordx4 v84, s[44:45]
	v_mfma_f32_32x32x16_f16 a[32:47], v[40:43], v[104:107], a[32:47]
	v_mfma_f32_32x32x16_f16 a[16:31], v[44:47], v[104:107], a[16:31]
	v_mfma_f32_32x32x16_f16 a[0:15], v[48:51], v[104:107], a[0:15]
	ds_read_b128 v[28:31], v98 offset:6144
	ds_read_b128 v[32:35], v98 offset:7168
	ds_read_b128 v[36:39], v98 offset:8192
	ds_read_b128 v[40:43], v98 offset:9216
	ds_read_b128 v[44:47], v98 offset:10240
	ds_read_b128 v[48:51], v98 offset:11264
	s_waitcnt lgkmcnt(6)
	v_mfma_f32_32x32x16_f16 a[80:95], v[4:7], v[108:111], a[80:95]
	s_waitcnt vmcnt(26)
	ds_write_b128 v81, v[148:151]
	ds_write_b128 v81, v[152:155] offset:1024
	ds_write_b128 v81, v[156:159] offset:2048
	ds_write_b128 v81, v[72:75] offset:3072
	v_mfma_f32_32x32x16_f16 a[64:79], v[8:11], v[108:111], a[64:79]
	ds_read_b128 v[52:55], v95
	ds_read_b128 v[56:59], v96
	ds_read_b128 v[60:63], v97
	ds_read_b128 v[0:3], v94
	v_mfma_f32_32x32x16_f16 a[48:63], v[12:15], v[108:111], a[48:63]
	global_load_dwordx4 v[148:151], v64, s[4:5] offset:1408
	global_load_dwordx4 v[152:155], v66, s[4:5] offset:1408
	global_load_dwordx4 v[156:159], v68, s[4:5] offset:1408
	global_load_dwordx4 v[72:75], v70, s[4:5] offset:1408
	s_waitcnt vmcnt(14)
	s_waitcnt lgkmcnt(8)
	s_barrier
	ds_read_b128 v[4:7], v84 offset:0
	ds_read_b128 v[8:11], v84 offset:1024
	ds_read_b128 v[12:15], v84 offset:2048
	v_mfma_f32_32x32x16_f16 a[32:47], v[16:19], v[108:111], a[32:47]
	ds_read_b128 v[16:19], v84 offset:3072
	v_mfma_f32_32x32x16_f16 a[16:31], v[20:23], v[108:111], a[16:31]
	ds_read_b128 v[20:23], v84 offset:4096
	v_mfma_f32_32x32x16_f16 a[0:15], v[24:27], v[108:111], a[0:15]
	ds_read_b128 v[24:27], v84 offset:5120
	v_mfma_f32_32x32x16_f16 a[80:95], v[28:31], v[112:115], a[80:95]
	s_add_u32 m0, s46, 0x103c0
	s_add_u32 s40, s40, 0x1800
	s_addc_u32 s41, s41, 0
	global_load_lds_dwordx4 v84, s[40:41]
	v_mfma_f32_32x32x16_f16 a[64:79], v[32:35], v[112:115], a[64:79]
	s_add_u32 m0, s47, 0x103c0
	s_add_u32 s42, s42, 0x1800
	s_addc_u32 s43, s43, 0
	global_load_lds_dwordx4 v84, s[42:43]
	v_mfma_f32_32x32x16_f16 a[48:63], v[36:39], v[112:115], a[48:63]
	s_add_u32 m0, s48, 0x103c0
	s_add_u32 s44, s44, 0x1800
	s_addc_u32 s45, s45, 0
	global_load_lds_dwordx4 v84, s[44:45]
	v_mfma_f32_32x32x16_f16 a[32:47], v[40:43], v[112:115], a[32:47]
	v_mfma_f32_32x32x16_f16 a[16:31], v[44:47], v[112:115], a[16:31]
	v_mfma_f32_32x32x16_f16 a[0:15], v[48:51], v[112:115], a[0:15]
	s_waitcnt lgkmcnt(6)
	ds_read_b128 v[28:31], v84 offset:6144
	ds_read_b128 v[32:35], v84 offset:7168
	ds_read_b128 v[36:39], v84 offset:8192
	ds_read_b128 v[40:43], v84 offset:9216
	ds_read_b128 v[44:47], v84 offset:10240
	ds_read_b128 v[48:51], v84 offset:11264
	s_waitcnt lgkmcnt(6)
	v_mfma_f32_32x32x16_f16 a[80:95], v[4:7], v[52:55], a[80:95]
	v_mfma_f32_32x32x16_f16 a[64:79], v[8:11], v[52:55], a[64:79]
	v_mfma_f32_32x32x16_f16 a[48:63], v[12:15], v[52:55], a[48:63]
	s_waitcnt vmcnt(10)
	s_waitcnt lgkmcnt(0)
	s_barrier
	ds_read_b128 v[4:7], v84 offset:12288
	ds_read_b128 v[8:11], v84 offset:13312
	ds_read_b128 v[12:15], v84 offset:14336
	v_mfma_f32_32x32x16_f16 a[32:47], v[16:19], v[52:55], a[32:47]
	ds_read_b128 v[16:19], v84 offset:15360
	v_mfma_f32_32x32x16_f16 a[16:31], v[20:23], v[52:55], a[16:31]
	ds_read_b128 v[20:23], v84 offset:16384
	v_mfma_f32_32x32x16_f16 a[0:15], v[24:27], v[52:55], a[0:15]
	ds_read_b128 v[24:27], v84 offset:17408
	v_mfma_f32_32x32x16_f16 a[80:95], v[28:31], v[56:59], a[80:95]
	s_add_u32 m0, s46, 0x0
	s_add_u32 s40, s40, 0x1800
	s_addc_u32 s41, s41, 0
	global_load_lds_dwordx4 v84, s[40:41]
	v_mfma_f32_32x32x16_f16 a[64:79], v[32:35], v[56:59], a[64:79]
	s_add_u32 m0, s47, 0x0
	s_add_u32 s42, s42, 0x1800
	s_addc_u32 s43, s43, 0
	global_load_lds_dwordx4 v84, s[42:43]
	v_mfma_f32_32x32x16_f16 a[48:63], v[36:39], v[56:59], a[48:63]
	s_add_u32 m0, s48, 0x0
	s_add_u32 s44, s44, 0x1800
	s_addc_u32 s45, s45, 0
	global_load_lds_dwordx4 v84, s[44:45]
	v_mfma_f32_32x32x16_f16 a[32:47], v[40:43], v[56:59], a[32:47]
	v_mfma_f32_32x32x16_f16 a[16:31], v[44:47], v[56:59], a[16:31]
	v_mfma_f32_32x32x16_f16 a[0:15], v[48:51], v[56:59], a[0:15]
	ds_read_b128 v[28:31], v84 offset:18432
	ds_read_b128 v[32:35], v84 offset:19456
	ds_read_b128 v[36:39], v84 offset:20480
	ds_read_b128 v[40:43], v84 offset:21504
	ds_read_b128 v[44:47], v84 offset:22528
	ds_read_b128 v[48:51], v84 offset:23552
	s_waitcnt lgkmcnt(6)
	v_mfma_f32_32x32x16_f16 a[80:95], v[4:7], v[60:63], a[80:95]
	s_waitcnt vmcnt(26)
	ds_write_b128 v81, v[116:119]
	ds_write_b128 v81, v[120:123] offset:1024
	ds_write_b128 v81, v[124:127] offset:2048
	ds_write_b128 v81, v[128:131] offset:3072
	v_mfma_f32_32x32x16_f16 a[64:79], v[8:11], v[60:63], a[64:79]
	ds_read_b128 v[100:103], v95
	ds_read_b128 v[104:107], v96
	ds_read_b128 v[108:111], v97
	ds_read_b128 v[112:115], v94
	v_mfma_f32_32x32x16_f16 a[48:63], v[12:15], v[60:63], a[48:63]
	global_load_dwordx4 v[116:119], v64, s[4:5] offset:1440
	global_load_dwordx4 v[120:123], v66, s[4:5] offset:1440
	global_load_dwordx4 v[124:127], v68, s[4:5] offset:1440
	global_load_dwordx4 v[128:131], v70, s[4:5] offset:1440
	s_waitcnt vmcnt(14)
	s_waitcnt lgkmcnt(8)
	s_barrier
	ds_read_b128 v[4:7], v84 offset:54208
	ds_read_b128 v[8:11], v84 offset:55232
	ds_read_b128 v[12:15], v84 offset:56256
	v_mfma_f32_32x32x16_f16 a[32:47], v[16:19], v[60:63], a[32:47]
	ds_read_b128 v[16:19], v84 offset:57280
	v_mfma_f32_32x32x16_f16 a[16:31], v[20:23], v[60:63], a[16:31]
	ds_read_b128 v[20:23], v84 offset:58304
	v_mfma_f32_32x32x16_f16 a[0:15], v[24:27], v[60:63], a[0:15]
	ds_read_b128 v[24:27], v84 offset:59328
	v_mfma_f32_32x32x16_f16 a[80:95], v[28:31], v[0:3], a[80:95]
	s_add_u32 m0, s46, 0x3000
	s_add_u32 s40, s40, 0x1800
	s_addc_u32 s41, s41, 0
	global_load_lds_dwordx4 v84, s[40:41]
	v_mfma_f32_32x32x16_f16 a[64:79], v[32:35], v[0:3], a[64:79]
	s_add_u32 m0, s47, 0x3000
	s_add_u32 s42, s42, 0x1800
	s_addc_u32 s43, s43, 0
	global_load_lds_dwordx4 v84, s[42:43]
	v_mfma_f32_32x32x16_f16 a[48:63], v[36:39], v[0:3], a[48:63]
	s_add_u32 m0, s48, 0x3000
	s_add_u32 s44, s44, 0x1800
	s_addc_u32 s45, s45, 0
	global_load_lds_dwordx4 v84, s[44:45]
	v_mfma_f32_32x32x16_f16 a[32:47], v[40:43], v[0:3], a[32:47]
	v_mfma_f32_32x32x16_f16 a[16:31], v[44:47], v[0:3], a[16:31]
	v_mfma_f32_32x32x16_f16 a[0:15], v[48:51], v[0:3], a[0:15]
	s_waitcnt lgkmcnt(6)
	ds_read_b128 v[28:31], v84 offset:60352
	ds_read_b128 v[32:35], v84 offset:61376
	ds_read_b128 v[36:39], v84 offset:62400
	ds_read_b128 v[40:43], v84 offset:63424
	ds_read_b128 v[44:47], v84 offset:64448
	ds_read_b128 v[48:51], v84 offset:65472
	s_waitcnt lgkmcnt(6)
	v_mfma_f32_32x32x16_f16 a[80:95], v[4:7], v[100:103], a[80:95]
	v_mfma_f32_32x32x16_f16 a[64:79], v[8:11], v[100:103], a[64:79]
	v_mfma_f32_32x32x16_f16 a[48:63], v[12:15], v[100:103], a[48:63]
	s_waitcnt vmcnt(10)
	s_waitcnt lgkmcnt(0)
	s_barrier
	ds_read_b128 v[4:7], v98
	ds_read_b128 v[8:11], v98 offset:1024
	ds_read_b128 v[12:15], v98 offset:2048
	v_mfma_f32_32x32x16_f16 a[32:47], v[16:19], v[100:103], a[32:47]
	ds_read_b128 v[16:19], v98 offset:3072
	v_mfma_f32_32x32x16_f16 a[16:31], v[20:23], v[100:103], a[16:31]
	ds_read_b128 v[20:23], v98 offset:4096
	v_mfma_f32_32x32x16_f16 a[0:15], v[24:27], v[100:103], a[0:15]
	ds_read_b128 v[24:27], v98 offset:5120
	v_mfma_f32_32x32x16_f16 a[80:95], v[28:31], v[104:107], a[80:95]
	s_add_u32 m0, s46, 0xd3c0
	s_add_u32 s40, s40, 0x1800
	s_addc_u32 s41, s41, 0
	global_load_lds_dwordx4 v84, s[40:41]
	v_mfma_f32_32x32x16_f16 a[64:79], v[32:35], v[104:107], a[64:79]
	s_add_u32 m0, s47, 0xd3c0
	s_add_u32 s42, s42, 0x1800
	s_addc_u32 s43, s43, 0
	global_load_lds_dwordx4 v84, s[42:43]
	v_mfma_f32_32x32x16_f16 a[48:63], v[36:39], v[104:107], a[48:63]
	s_add_u32 m0, s48, 0xd3c0
	s_add_u32 s44, s44, 0x1800
	s_addc_u32 s45, s45, 0
	global_load_lds_dwordx4 v84, s[44:45]
	v_mfma_f32_32x32x16_f16 a[32:47], v[40:43], v[104:107], a[32:47]
	v_mfma_f32_32x32x16_f16 a[16:31], v[44:47], v[104:107], a[16:31]
	v_mfma_f32_32x32x16_f16 a[0:15], v[48:51], v[104:107], a[0:15]
	ds_read_b128 v[28:31], v98 offset:6144
	ds_read_b128 v[32:35], v98 offset:7168
	ds_read_b128 v[36:39], v98 offset:8192
	ds_read_b128 v[40:43], v98 offset:9216
	ds_read_b128 v[44:47], v98 offset:10240
	ds_read_b128 v[48:51], v98 offset:11264
	s_waitcnt lgkmcnt(6)
	v_mfma_f32_32x32x16_f16 a[80:95], v[4:7], v[108:111], a[80:95]
	s_waitcnt vmcnt(26)
	ds_write_b128 v81, v[132:135]
	ds_write_b128 v81, v[136:139] offset:1024
	ds_write_b128 v81, v[140:143] offset:2048
	ds_write_b128 v81, v[144:147] offset:3072
	v_mfma_f32_32x32x16_f16 a[64:79], v[8:11], v[108:111], a[64:79]
	ds_read_b128 v[52:55], v95
	ds_read_b128 v[56:59], v96
	ds_read_b128 v[60:63], v97
	ds_read_b128 v[0:3], v94
	v_mfma_f32_32x32x16_f16 a[48:63], v[12:15], v[108:111], a[48:63]
	s_waitcnt vmcnt(10)
	s_waitcnt lgkmcnt(8)
	s_barrier
	ds_read_b128 v[4:7], v84 offset:0
	ds_read_b128 v[8:11], v84 offset:1024
	ds_read_b128 v[12:15], v84 offset:2048
	v_mfma_f32_32x32x16_f16 a[32:47], v[16:19], v[108:111], a[32:47]
	ds_read_b128 v[16:19], v84 offset:3072
	v_mfma_f32_32x32x16_f16 a[16:31], v[20:23], v[108:111], a[16:31]
	ds_read_b128 v[20:23], v84 offset:4096
	v_mfma_f32_32x32x16_f16 a[0:15], v[24:27], v[108:111], a[0:15]
	ds_read_b128 v[24:27], v84 offset:5120
	v_mfma_f32_32x32x16_f16 a[80:95], v[28:31], v[112:115], a[80:95]
	s_add_u32 m0, s46, 0x103c0
	s_add_u32 s40, s40, 0x1800
	s_addc_u32 s41, s41, 0
	global_load_lds_dwordx4 v84, s[40:41]
	v_mfma_f32_32x32x16_f16 a[64:79], v[32:35], v[112:115], a[64:79]
	s_add_u32 m0, s47, 0x103c0
	s_add_u32 s42, s42, 0x1800
	s_addc_u32 s43, s43, 0
	global_load_lds_dwordx4 v84, s[42:43]
	v_mfma_f32_32x32x16_f16 a[48:63], v[36:39], v[112:115], a[48:63]
	s_add_u32 m0, s48, 0x103c0
	s_add_u32 s44, s44, 0x1800
	s_addc_u32 s45, s45, 0
	global_load_lds_dwordx4 v84, s[44:45]
	v_mfma_f32_32x32x16_f16 a[32:47], v[40:43], v[112:115], a[32:47]
	v_mfma_f32_32x32x16_f16 a[16:31], v[44:47], v[112:115], a[16:31]
	v_mfma_f32_32x32x16_f16 a[0:15], v[48:51], v[112:115], a[0:15]
	s_waitcnt lgkmcnt(6)
	ds_read_b128 v[28:31], v84 offset:6144
	ds_read_b128 v[32:35], v84 offset:7168
	ds_read_b128 v[36:39], v84 offset:8192
	ds_read_b128 v[40:43], v84 offset:9216
	ds_read_b128 v[44:47], v84 offset:10240
	ds_read_b128 v[48:51], v84 offset:11264
	s_waitcnt lgkmcnt(6)
	v_mfma_f32_32x32x16_f16 a[80:95], v[4:7], v[52:55], a[80:95]
	v_mfma_f32_32x32x16_f16 a[64:79], v[8:11], v[52:55], a[64:79]
	v_mfma_f32_32x32x16_f16 a[48:63], v[12:15], v[52:55], a[48:63]
	s_waitcnt vmcnt(6)
	s_waitcnt lgkmcnt(0)
	s_barrier
	ds_read_b128 v[4:7], v84 offset:12288
	ds_read_b128 v[8:11], v84 offset:13312
	ds_read_b128 v[12:15], v84 offset:14336
	v_mfma_f32_32x32x16_f16 a[32:47], v[16:19], v[52:55], a[32:47]
	ds_read_b128 v[16:19], v84 offset:15360
	v_mfma_f32_32x32x16_f16 a[16:31], v[20:23], v[52:55], a[16:31]
	ds_read_b128 v[20:23], v84 offset:16384
	v_mfma_f32_32x32x16_f16 a[0:15], v[24:27], v[52:55], a[0:15]
	ds_read_b128 v[24:27], v84 offset:17408
	v_mfma_f32_32x32x16_f16 a[80:95], v[28:31], v[56:59], a[80:95]
	s_add_u32 m0, s46, 0x0
	s_add_u32 s40, s40, 0x1800
	s_addc_u32 s41, s41, 0
	global_load_lds_dwordx4 v84, s[40:41]
	v_mfma_f32_32x32x16_f16 a[64:79], v[32:35], v[56:59], a[64:79]
	s_add_u32 m0, s47, 0x0
	s_add_u32 s42, s42, s49
	s_addc_u32 s43, s43, 0
	global_load_lds_dwordx4 v84, s[42:43]
	v_mfma_f32_32x32x16_f16 a[48:63], v[36:39], v[56:59], a[48:63]
	s_add_u32 m0, s48, 0x0
	s_add_u32 s44, s44, 0xc00
	s_addc_u32 s45, s45, 0
	global_load_lds_dwordx4 v84, s[44:45]
	v_mfma_f32_32x32x16_f16 a[32:47], v[40:43], v[56:59], a[32:47]
	v_mfma_f32_32x32x16_f16 a[16:31], v[44:47], v[56:59], a[16:31]
	v_mfma_f32_32x32x16_f16 a[0:15], v[48:51], v[56:59], a[0:15]
	ds_read_b128 v[28:31], v84 offset:18432
	ds_read_b128 v[32:35], v84 offset:19456
	ds_read_b128 v[36:39], v84 offset:20480
	ds_read_b128 v[40:43], v84 offset:21504
	ds_read_b128 v[44:47], v84 offset:22528
	ds_read_b128 v[48:51], v84 offset:23552
	s_waitcnt lgkmcnt(6)
	v_mfma_f32_32x32x16_f16 a[80:95], v[4:7], v[60:63], a[80:95]
	s_waitcnt vmcnt(22)
	ds_write_b128 v81, v[148:151]
	ds_write_b128 v81, v[152:155] offset:1024
	ds_write_b128 v81, v[156:159] offset:2048
	ds_write_b128 v81, v[72:75] offset:3072
	v_mfma_f32_32x32x16_f16 a[64:79], v[8:11], v[60:63], a[64:79]
	ds_read_b128 v[100:103], v95
	ds_read_b128 v[104:107], v96
	ds_read_b128 v[108:111], v97
	ds_read_b128 v[112:115], v94
	v_mfma_f32_32x32x16_f16 a[48:63], v[12:15], v[60:63], a[48:63]
	s_waitcnt vmcnt(6)
	s_waitcnt lgkmcnt(8)
	s_barrier
	ds_read_b128 v[4:7], v84 offset:54208
	ds_read_b128 v[8:11], v84 offset:55232
	ds_read_b128 v[12:15], v84 offset:56256
	v_mfma_f32_32x32x16_f16 a[32:47], v[16:19], v[60:63], a[32:47]
	ds_read_b128 v[16:19], v84 offset:57280
	v_mfma_f32_32x32x16_f16 a[16:31], v[20:23], v[60:63], a[16:31]
	ds_read_b128 v[20:23], v84 offset:58304
	v_mfma_f32_32x32x16_f16 a[0:15], v[24:27], v[60:63], a[0:15]
	ds_read_b128 v[24:27], v84 offset:59328
	v_mfma_f32_32x32x16_f16 a[80:95], v[28:31], v[0:3], a[80:95]
	v_mfma_f32_32x32x16_f16 a[64:79], v[32:35], v[0:3], a[64:79]
	v_mfma_f32_32x32x16_f16 a[48:63], v[36:39], v[0:3], a[48:63]
	v_mfma_f32_32x32x16_f16 a[32:47], v[40:43], v[0:3], a[32:47]
	v_mfma_f32_32x32x16_f16 a[16:31], v[44:47], v[0:3], a[16:31]
	v_mfma_f32_32x32x16_f16 a[0:15], v[48:51], v[0:3], a[0:15]
	s_waitcnt lgkmcnt(6)
	ds_read_b128 v[28:31], v84 offset:60352
	ds_read_b128 v[32:35], v84 offset:61376
	ds_read_b128 v[36:39], v84 offset:62400
	ds_read_b128 v[40:43], v84 offset:63424
	ds_read_b128 v[44:47], v84 offset:64448
	ds_read_b128 v[48:51], v84 offset:65472
	s_waitcnt lgkmcnt(6)
	v_mfma_f32_32x32x16_f16 a[80:95], v[4:7], v[100:103], a[80:95]
	v_mfma_f32_32x32x16_f16 a[64:79], v[8:11], v[100:103], a[64:79]
	v_mfma_f32_32x32x16_f16 a[48:63], v[12:15], v[100:103], a[48:63]
	s_waitcnt vmcnt(3)
	s_waitcnt lgkmcnt(0)
	s_barrier
	ds_read_b128 v[4:7], v98
	ds_read_b128 v[8:11], v98 offset:1024
	ds_read_b128 v[12:15], v98 offset:2048
	v_mfma_f32_32x32x16_f16 a[32:47], v[16:19], v[100:103], a[32:47]
	ds_read_b128 v[16:19], v98 offset:3072
	v_mfma_f32_32x32x16_f16 a[16:31], v[20:23], v[100:103], a[16:31]
	ds_read_b128 v[20:23], v98 offset:4096
	v_mfma_f32_32x32x16_f16 a[0:15], v[24:27], v[100:103], a[0:15]
	ds_read_b128 v[24:27], v98 offset:5120
	v_mfma_f32_32x32x16_f16 a[80:95], v[28:31], v[104:107], a[80:95]
	v_mfma_f32_32x32x16_f16 a[64:79], v[32:35], v[104:107], a[64:79]
	v_mfma_f32_32x32x16_f16 a[48:63], v[36:39], v[104:107], a[48:63]
	v_mfma_f32_32x32x16_f16 a[32:47], v[40:43], v[104:107], a[32:47]
	v_mfma_f32_32x32x16_f16 a[16:31], v[44:47], v[104:107], a[16:31]
	v_mfma_f32_32x32x16_f16 a[0:15], v[48:51], v[104:107], a[0:15]
	ds_read_b128 v[28:31], v98 offset:6144
	ds_read_b128 v[32:35], v98 offset:7168
	ds_read_b128 v[36:39], v98 offset:8192
	ds_read_b128 v[40:43], v98 offset:9216
	ds_read_b128 v[44:47], v98 offset:10240
	ds_read_b128 v[48:51], v98 offset:11264
	s_waitcnt lgkmcnt(6)
	v_mfma_f32_32x32x16_f16 a[80:95], v[4:7], v[108:111], a[80:95]
	s_waitcnt vmcnt(12)
	ds_write_b128 v81, v[116:119]
	ds_write_b128 v81, v[120:123] offset:1024
	ds_write_b128 v81, v[124:127] offset:2048
	ds_write_b128 v81, v[128:131] offset:3072
	v_mfma_f32_32x32x16_f16 a[64:79], v[8:11], v[108:111], a[64:79]
	ds_read_b128 v[0:3], v94
	v_mfma_f32_32x32x16_f16 a[48:63], v[12:15], v[108:111], a[48:63]
	s_waitcnt vmcnt(0)
	s_waitcnt lgkmcnt(5)
	s_barrier
	ds_read_b128 v[4:7], v84 offset:0
	ds_read_b128 v[8:11], v84 offset:1024
	ds_read_b128 v[12:15], v84 offset:2048
	v_mfma_f32_32x32x16_f16 a[32:47], v[16:19], v[108:111], a[32:47]
	ds_read_b128 v[16:19], v84 offset:3072
	v_mfma_f32_32x32x16_f16 a[16:31], v[20:23], v[108:111], a[16:31]
	ds_read_b128 v[20:23], v84 offset:4096
	v_mfma_f32_32x32x16_f16 a[0:15], v[24:27], v[108:111], a[0:15]
	ds_read_b128 v[24:27], v84 offset:5120
	v_mfma_f32_32x32x16_f16 a[80:95], v[28:31], v[112:115], a[80:95]
	v_mfma_f32_32x32x16_f16 a[64:79], v[32:35], v[112:115], a[64:79]
	v_mfma_f32_32x32x16_f16 a[48:63], v[36:39], v[112:115], a[48:63]
	v_mfma_f32_32x32x16_f16 a[32:47], v[40:43], v[112:115], a[32:47]
	v_mfma_f32_32x32x16_f16 a[16:31], v[44:47], v[112:115], a[16:31]
	v_mfma_f32_32x32x16_f16 a[0:15], v[48:51], v[112:115], a[0:15]
	s_waitcnt lgkmcnt(0)
	v_mfma_f32_32x32x16_f16 a[80:95], v[4:7], v[0:3], a[80:95]
	v_mfma_f32_32x32x16_f16 a[16:31], v[20:23], v[0:3], a[16:31]
	v_lshlrev_b32_e32 v22, 4, v85
	v_mfma_f32_32x32x16_f16 a[64:79], v[8:11], v[0:3], a[64:79]
	v_mfma_f32_32x32x16_f16 a[48:63], v[12:15], v[0:3], a[48:63]
	s_nop 7
	v_accvgpr_read_b32 v13, a88
	v_mfma_f32_32x32x16_f16 a[32:47], v[16:19], v[0:3], a[32:47]
	v_accvgpr_read_b32 v17, a92
	v_mfma_f32_32x32x16_f16 a[0:15], v[24:27], v[0:3], a[0:15]
	ds_read_b128 v[2:5], v22 offset:53248
	ds_read_b128 v[6:9], v22 offset:53280
	v_accvgpr_read_b32 v1, a80
	v_lshlrev_b32_e32 v0, 4, v92
	s_waitcnt lgkmcnt(1)
	v_add_f32_e32 v1, v1, v2
	v_accvgpr_read_b32 v2, a81
	v_add_f32_e32 v2, v3, v2
	v_max_f32_e32 v10, 0, v2
	v_accvgpr_read_b32 v2, a82
	v_add_f32_e32 v2, v4, v2
	v_max_f32_e32 v11, 0, v2
	v_accvgpr_read_b32 v2, a83
	v_add_f32_e32 v2, v5, v2
	v_max_f32_e32 v12, 0, v2
	v_accvgpr_read_b32 v2, a84
	s_waitcnt lgkmcnt(0)
	v_add_f32_e32 v2, v2, v6
	v_max_f32_e32 v6, 0, v2
	v_accvgpr_read_b32 v2, a85
	v_add_f32_e32 v2, v7, v2
	v_max_f32_e32 v7, 0, v2
	v_accvgpr_read_b32 v2, a86
	v_add_f32_e32 v2, v8, v2
	v_max_f32_e32 v8, 0, v2
	v_accvgpr_read_b32 v2, a87
	v_add_f32_e32 v2, v9, v2
	v_max_f32_e32 v9, 0, v2
	ds_read_b128 v[2:5], v22 offset:53312
	v_max_f32_e32 v1, 0, v1
	s_waitcnt lgkmcnt(0)
	v_add_f32_e32 v2, v13, v2
	v_max_f32_e32 v13, 0, v2
	v_accvgpr_read_b32 v2, a89
	v_add_f32_e32 v2, v3, v2
	v_max_f32_e32 v14, 0, v2
	v_accvgpr_read_b32 v2, a90
	v_add_f32_e32 v2, v4, v2
	v_max_f32_e32 v15, 0, v2
	v_accvgpr_read_b32 v2, a91
	v_add_f32_e32 v2, v5, v2
	v_max_f32_e32 v16, 0, v2
	ds_read_b128 v[2:5], v22 offset:53344
	s_waitcnt lgkmcnt(0)
	v_add_f32_e32 v2, v17, v2
	v_max_f32_e32 v17, 0, v2
	v_accvgpr_read_b32 v2, a93
	v_add_f32_e32 v2, v3, v2
	v_max_f32_e32 v18, 0, v2
	v_accvgpr_read_b32 v2, a94
	v_add_f32_e32 v2, v4, v2
	v_max_f32_e32 v19, 0, v2
	v_accvgpr_read_b32 v2, a95
	v_add_f32_e32 v2, v5, v2
	v_cvt_pk_f16_f32 v5, v8, v9
	v_cvt_pk_f16_f32 v4, v6, v7
	ds_read_b128 v[6:9], v0 offset:40960
	v_max_f32_e32 v20, 0, v2
	v_cvt_pk_f16_f32 v3, v11, v12
	v_cvt_pk_f16_f32 v2, v1, v10
	v_accvgpr_read_b32 v1, a64
	s_waitcnt lgkmcnt(0)
	v_mfma_f32_32x32x16_f16 a[80:95], v[6:9], v[2:5], 0
	ds_read_b128 v[6:9], v0 offset:41984
	v_cvt_pk_f16_f32 v5, v19, v20
	v_cvt_pk_f16_f32 v4, v17, v18
	v_cvt_pk_f16_f32 v3, v15, v16
	v_cvt_pk_f16_f32 v2, v13, v14
	v_accvgpr_read_b32 v13, a72
	v_accvgpr_read_b32 v17, a76
	s_waitcnt lgkmcnt(0)
	v_mfma_f32_32x32x16_f16 a[80:95], v[6:9], v[2:5], a[80:95]
	ds_read_b128 v[2:5], v22 offset:53376
	v_accvgpr_read_b32 v9, a68
	s_waitcnt lgkmcnt(0)
	v_add_f32_e32 v1, v1, v2
	v_accvgpr_read_b32 v2, a65
	v_add_f32_e32 v2, v3, v2
	v_max_f32_e32 v6, 0, v2
	v_accvgpr_read_b32 v2, a66
	v_add_f32_e32 v2, v4, v2
	v_max_f32_e32 v7, 0, v2
	v_accvgpr_read_b32 v2, a67
	v_add_f32_e32 v2, v5, v2
	v_max_f32_e32 v8, 0, v2
	ds_read_b128 v[2:5], v22 offset:53408
	v_max_f32_e32 v1, 0, v1
	s_waitcnt lgkmcnt(0)
	v_add_f32_e32 v2, v9, v2
	v_max_f32_e32 v9, 0, v2
	v_accvgpr_read_b32 v2, a69
	v_add_f32_e32 v2, v3, v2
	v_max_f32_e32 v10, 0, v2
	v_accvgpr_read_b32 v2, a70
	v_add_f32_e32 v2, v4, v2
	v_max_f32_e32 v11, 0, v2
	v_accvgpr_read_b32 v2, a71
	v_add_f32_e32 v2, v5, v2
	v_max_f32_e32 v12, 0, v2
	ds_read_b128 v[2:5], v22 offset:53440
	s_waitcnt lgkmcnt(0)
	v_add_f32_e32 v2, v13, v2
	v_max_f32_e32 v13, 0, v2
	v_accvgpr_read_b32 v2, a73
	v_add_f32_e32 v2, v3, v2
	v_max_f32_e32 v14, 0, v2
	v_accvgpr_read_b32 v2, a74
	v_add_f32_e32 v2, v4, v2
	v_max_f32_e32 v15, 0, v2
	v_accvgpr_read_b32 v2, a75
	v_add_f32_e32 v2, v5, v2
	v_max_f32_e32 v16, 0, v2
	ds_read_b128 v[2:5], v22 offset:53472
	s_waitcnt lgkmcnt(0)
	v_add_f32_e32 v2, v17, v2
	v_max_f32_e32 v17, 0, v2
	v_accvgpr_read_b32 v2, a77
	v_add_f32_e32 v2, v3, v2
	v_max_f32_e32 v18, 0, v2
	v_accvgpr_read_b32 v2, a78
	v_add_f32_e32 v2, v4, v2
	v_max_f32_e32 v19, 0, v2
	v_accvgpr_read_b32 v2, a79
	v_add_f32_e32 v2, v5, v2
	v_max_f32_e32 v20, 0, v2
	v_cvt_pk_f16_f32 v4, v9, v10
	v_cvt_pk_f16_f32 v3, v7, v8
	v_cvt_pk_f16_f32 v2, v1, v6
	ds_read_b128 v[6:9], v0 offset:43008
	v_cvt_pk_f16_f32 v5, v11, v12
	v_accvgpr_read_b32 v1, a48
	s_waitcnt lgkmcnt(0)
	v_mfma_f32_32x32x16_f16 a[80:95], v[6:9], v[2:5], a[80:95]
	ds_read_b128 v[6:9], v0 offset:44032
	v_cvt_pk_f16_f32 v5, v19, v20
	v_cvt_pk_f16_f32 v4, v17, v18
	v_cvt_pk_f16_f32 v3, v15, v16
	v_cvt_pk_f16_f32 v2, v13, v14
	v_accvgpr_read_b32 v13, a56
	v_accvgpr_read_b32 v17, a60
	s_waitcnt lgkmcnt(0)
	v_mfma_f32_32x32x16_f16 a[80:95], v[6:9], v[2:5], a[80:95]
	ds_read_b128 v[2:5], v22 offset:53504
	v_accvgpr_read_b32 v9, a52
	s_waitcnt lgkmcnt(0)
	v_add_f32_e32 v1, v1, v2
	v_accvgpr_read_b32 v2, a49
	v_add_f32_e32 v2, v3, v2
	v_max_f32_e32 v6, 0, v2
	v_accvgpr_read_b32 v2, a50
	v_add_f32_e32 v2, v4, v2
	v_max_f32_e32 v7, 0, v2
	v_accvgpr_read_b32 v2, a51
	v_add_f32_e32 v2, v5, v2
	v_max_f32_e32 v8, 0, v2
	ds_read_b128 v[2:5], v22 offset:53536
	v_max_f32_e32 v1, 0, v1
	s_waitcnt lgkmcnt(0)
	v_add_f32_e32 v2, v9, v2
	v_max_f32_e32 v9, 0, v2
	v_accvgpr_read_b32 v2, a53
	v_add_f32_e32 v2, v3, v2
	v_max_f32_e32 v10, 0, v2
	v_accvgpr_read_b32 v2, a54
	v_add_f32_e32 v2, v4, v2
	v_max_f32_e32 v11, 0, v2
	v_accvgpr_read_b32 v2, a55
	v_add_f32_e32 v2, v5, v2
	v_max_f32_e32 v12, 0, v2
	ds_read_b128 v[2:5], v22 offset:53568
	s_waitcnt lgkmcnt(0)
	v_add_f32_e32 v2, v13, v2
	v_max_f32_e32 v13, 0, v2
	v_accvgpr_read_b32 v2, a57
	v_add_f32_e32 v2, v3, v2
	v_max_f32_e32 v14, 0, v2
	v_accvgpr_read_b32 v2, a58
	v_add_f32_e32 v2, v4, v2
	v_max_f32_e32 v15, 0, v2
	v_accvgpr_read_b32 v2, a59
	v_add_f32_e32 v2, v5, v2
	v_max_f32_e32 v16, 0, v2
	ds_read_b128 v[2:5], v22 offset:53600
	s_waitcnt lgkmcnt(0)
	v_add_f32_e32 v2, v17, v2
	v_max_f32_e32 v17, 0, v2
	v_accvgpr_read_b32 v2, a61
	v_add_f32_e32 v2, v3, v2
	v_max_f32_e32 v18, 0, v2
	v_accvgpr_read_b32 v2, a62
	v_add_f32_e32 v2, v4, v2
	v_max_f32_e32 v19, 0, v2
	v_accvgpr_read_b32 v2, a63
	v_add_f32_e32 v2, v5, v2
	v_max_f32_e32 v20, 0, v2
	v_cvt_pk_f16_f32 v4, v9, v10
	v_cvt_pk_f16_f32 v3, v7, v8
	v_cvt_pk_f16_f32 v2, v1, v6
	ds_read_b128 v[6:9], v0 offset:45056
	v_cvt_pk_f16_f32 v5, v11, v12
	v_accvgpr_read_b32 v1, a32
	s_waitcnt lgkmcnt(0)
	v_mfma_f32_32x32x16_f16 a[80:95], v[6:9], v[2:5], a[80:95]
	ds_read_b128 v[6:9], v0 offset:46080
	v_cvt_pk_f16_f32 v5, v19, v20
	v_cvt_pk_f16_f32 v4, v17, v18
	v_cvt_pk_f16_f32 v3, v15, v16
	v_cvt_pk_f16_f32 v2, v13, v14
	v_accvgpr_read_b32 v13, a40
	v_accvgpr_read_b32 v17, a44
	s_waitcnt lgkmcnt(0)
	v_mfma_f32_32x32x16_f16 a[80:95], v[6:9], v[2:5], a[80:95]
	ds_read_b128 v[2:5], v22 offset:53632
	v_accvgpr_read_b32 v9, a36
	s_waitcnt lgkmcnt(0)
	v_add_f32_e32 v1, v1, v2
	v_accvgpr_read_b32 v2, a33
	v_add_f32_e32 v2, v3, v2
	v_max_f32_e32 v6, 0, v2
	v_accvgpr_read_b32 v2, a34
	v_add_f32_e32 v2, v4, v2
	v_max_f32_e32 v7, 0, v2
	v_accvgpr_read_b32 v2, a35
	v_add_f32_e32 v2, v5, v2
	v_max_f32_e32 v8, 0, v2
	ds_read_b128 v[2:5], v22 offset:53664
	v_max_f32_e32 v1, 0, v1
	s_waitcnt lgkmcnt(0)
	v_add_f32_e32 v2, v9, v2
	v_max_f32_e32 v9, 0, v2
	v_accvgpr_read_b32 v2, a37
	v_add_f32_e32 v2, v3, v2
	v_max_f32_e32 v10, 0, v2
	v_accvgpr_read_b32 v2, a38
	v_add_f32_e32 v2, v4, v2
	v_max_f32_e32 v11, 0, v2
	v_accvgpr_read_b32 v2, a39
	v_add_f32_e32 v2, v5, v2
	v_max_f32_e32 v12, 0, v2
	ds_read_b128 v[2:5], v22 offset:53696
	s_waitcnt lgkmcnt(0)
	v_add_f32_e32 v2, v13, v2
	v_max_f32_e32 v13, 0, v2
	v_accvgpr_read_b32 v2, a41
	v_add_f32_e32 v2, v3, v2
	v_max_f32_e32 v14, 0, v2
	v_accvgpr_read_b32 v2, a42
	v_add_f32_e32 v2, v4, v2
	v_max_f32_e32 v15, 0, v2
	v_accvgpr_read_b32 v2, a43
	v_add_f32_e32 v2, v5, v2
	v_max_f32_e32 v16, 0, v2
	ds_read_b128 v[2:5], v22 offset:53728
	s_waitcnt lgkmcnt(0)
	v_add_f32_e32 v2, v17, v2
	v_max_f32_e32 v17, 0, v2
	v_accvgpr_read_b32 v2, a45
	v_add_f32_e32 v2, v3, v2
	v_max_f32_e32 v18, 0, v2
	v_accvgpr_read_b32 v2, a46
	v_add_f32_e32 v2, v4, v2
	v_max_f32_e32 v19, 0, v2
	v_accvgpr_read_b32 v2, a47
	v_add_f32_e32 v2, v5, v2
	v_max_f32_e32 v20, 0, v2
	v_cvt_pk_f16_f32 v4, v9, v10
	v_cvt_pk_f16_f32 v3, v7, v8
	v_cvt_pk_f16_f32 v2, v1, v6
	ds_read_b128 v[6:9], v0 offset:47104
	v_cvt_pk_f16_f32 v5, v11, v12
	v_accvgpr_read_b32 v1, a16
	s_waitcnt lgkmcnt(0)
	v_mfma_f32_32x32x16_f16 a[32:47], v[6:9], v[2:5], 0
	ds_read_b128 v[6:9], v0 offset:48128
	v_cvt_pk_f16_f32 v5, v19, v20
	v_cvt_pk_f16_f32 v4, v17, v18
	v_cvt_pk_f16_f32 v3, v15, v16
	v_cvt_pk_f16_f32 v2, v13, v14
	v_accvgpr_read_b32 v13, a24
	v_accvgpr_read_b32 v17, a28
	s_waitcnt lgkmcnt(0)
	v_mfma_f32_32x32x16_f16 a[32:47], v[6:9], v[2:5], a[32:47]
	ds_read_b128 v[2:5], v22 offset:53760
	v_accvgpr_read_b32 v9, a20
	s_waitcnt lgkmcnt(0)
	v_add_f32_e32 v1, v1, v2
	v_accvgpr_read_b32 v2, a17
	v_add_f32_e32 v2, v3, v2
	v_max_f32_e32 v6, 0, v2
	v_accvgpr_read_b32 v2, a18
	v_add_f32_e32 v2, v4, v2
	v_max_f32_e32 v7, 0, v2
	v_accvgpr_read_b32 v2, a19
	v_add_f32_e32 v2, v5, v2
	v_max_f32_e32 v8, 0, v2
	ds_read_b128 v[2:5], v22 offset:53792
	v_max_f32_e32 v1, 0, v1
	s_waitcnt lgkmcnt(0)
	v_add_f32_e32 v2, v9, v2
	v_max_f32_e32 v9, 0, v2
	v_accvgpr_read_b32 v2, a21
	v_add_f32_e32 v2, v3, v2
	v_max_f32_e32 v10, 0, v2
	v_accvgpr_read_b32 v2, a22
	v_add_f32_e32 v2, v4, v2
	v_max_f32_e32 v11, 0, v2
	v_accvgpr_read_b32 v2, a23
	v_add_f32_e32 v2, v5, v2
	v_max_f32_e32 v12, 0, v2
	ds_read_b128 v[2:5], v22 offset:53824
	s_waitcnt lgkmcnt(0)
	v_add_f32_e32 v2, v13, v2
	v_max_f32_e32 v13, 0, v2
	v_accvgpr_read_b32 v2, a25
	v_add_f32_e32 v2, v3, v2
	v_max_f32_e32 v14, 0, v2
	v_accvgpr_read_b32 v2, a26
	v_add_f32_e32 v2, v4, v2
	v_max_f32_e32 v15, 0, v2
	v_accvgpr_read_b32 v2, a27
	v_add_f32_e32 v2, v5, v2
	v_max_f32_e32 v16, 0, v2
	ds_read_b128 v[2:5], v22 offset:53856
	s_waitcnt lgkmcnt(0)
	v_add_f32_e32 v2, v17, v2
	v_max_f32_e32 v17, 0, v2
	v_accvgpr_read_b32 v2, a29
	v_add_f32_e32 v2, v3, v2
	v_max_f32_e32 v18, 0, v2
	v_accvgpr_read_b32 v2, a30
	v_add_f32_e32 v2, v4, v2
	v_max_f32_e32 v19, 0, v2
	v_accvgpr_read_b32 v2, a31
	v_add_f32_e32 v2, v5, v2
	v_max_f32_e32 v20, 0, v2
	v_cvt_pk_f16_f32 v4, v9, v10
	v_cvt_pk_f16_f32 v3, v7, v8
	v_cvt_pk_f16_f32 v2, v1, v6
	ds_read_b128 v[6:9], v0 offset:49152
	v_cvt_pk_f16_f32 v5, v11, v12
	v_accvgpr_read_b32 v1, a0
	s_waitcnt lgkmcnt(0)
	v_mfma_f32_32x32x16_f16 a[32:47], v[6:9], v[2:5], a[32:47]
	ds_read_b128 v[6:9], v0 offset:50176
	v_cvt_pk_f16_f32 v5, v19, v20
	v_cvt_pk_f16_f32 v4, v17, v18
	v_cvt_pk_f16_f32 v3, v15, v16
	v_cvt_pk_f16_f32 v2, v13, v14
	v_accvgpr_read_b32 v13, a8
	v_accvgpr_read_b32 v17, a12
	s_waitcnt lgkmcnt(0)
	v_mfma_f32_32x32x16_f16 a[32:47], v[6:9], v[2:5], a[32:47]
	ds_read_b128 v[2:5], v22 offset:53888
	v_accvgpr_read_b32 v9, a4
	s_waitcnt lgkmcnt(0)
	v_add_f32_e32 v1, v1, v2
	v_accvgpr_read_b32 v2, a1
	v_add_f32_e32 v2, v3, v2
	v_max_f32_e32 v6, 0, v2
	v_accvgpr_read_b32 v2, a2
	v_add_f32_e32 v2, v4, v2
	v_max_f32_e32 v7, 0, v2
	v_accvgpr_read_b32 v2, a3
	v_add_f32_e32 v2, v5, v2
	v_max_f32_e32 v8, 0, v2
	ds_read_b128 v[2:5], v22 offset:53920
	v_max_f32_e32 v1, 0, v1
	s_waitcnt lgkmcnt(0)
	v_add_f32_e32 v2, v9, v2
	v_max_f32_e32 v9, 0, v2
	v_accvgpr_read_b32 v2, a5
	v_add_f32_e32 v2, v3, v2
	v_max_f32_e32 v10, 0, v2
	v_accvgpr_read_b32 v2, a6
	v_add_f32_e32 v2, v4, v2
	v_max_f32_e32 v11, 0, v2
	v_accvgpr_read_b32 v2, a7
	v_add_f32_e32 v2, v5, v2
	v_max_f32_e32 v12, 0, v2
	ds_read_b128 v[2:5], v22 offset:53952
	s_waitcnt lgkmcnt(0)
	v_add_f32_e32 v2, v13, v2
	v_max_f32_e32 v13, 0, v2
	v_accvgpr_read_b32 v2, a9
	v_add_f32_e32 v2, v3, v2
	v_max_f32_e32 v14, 0, v2
	v_accvgpr_read_b32 v2, a10
	v_add_f32_e32 v2, v4, v2
	v_max_f32_e32 v15, 0, v2
	v_accvgpr_read_b32 v2, a11
	v_add_f32_e32 v2, v5, v2
	v_max_f32_e32 v16, 0, v2
	ds_read_b128 v[2:5], v22 offset:53984
	s_waitcnt lgkmcnt(0)
	v_add_f32_e32 v2, v17, v2
	v_max_f32_e32 v17, 0, v2
	v_accvgpr_read_b32 v2, a13
	v_add_f32_e32 v2, v3, v2
	v_max_f32_e32 v18, 0, v2
	v_accvgpr_read_b32 v2, a14
	v_add_f32_e32 v2, v4, v2
	v_max_f32_e32 v19, 0, v2
	v_accvgpr_read_b32 v2, a15
	v_add_f32_e32 v2, v5, v2
	v_max_f32_e32 v20, 0, v2
	v_cvt_pk_f16_f32 v4, v9, v10
	v_cvt_pk_f16_f32 v3, v7, v8
	v_cvt_pk_f16_f32 v2, v1, v6
	ds_read_b128 v[6:9], v0 offset:51200
	v_cvt_pk_f16_f32 v5, v11, v12
	s_waitcnt lgkmcnt(0)
	s_nop 0
	v_mfma_f32_32x32x16_f16 a[32:47], v[6:9], v[2:5], a[32:47]
	ds_read_b128 v[6:9], v0 offset:52224
	v_cvt_pk_f16_f32 v5, v19, v20
	v_cvt_pk_f16_f32 v4, v17, v18
	v_cvt_pk_f16_f32 v3, v15, v16
	v_cvt_pk_f16_f32 v2, v13, v14
	s_waitcnt lgkmcnt(0)
	s_nop 0
	v_mfma_f32_32x32x16_f16 a[32:47], v[6:9], v[2:5], a[32:47]
	s_and_saveexec_b64 s[2:3], s[0:1]
	s_cbranch_execz .LBB3_39
	v_accvgpr_read_b32 v0, a80
	v_accvgpr_read_b32 v6, a86
	v_accvgpr_read_b32 v7, a87
	v_accvgpr_read_b32 v8, a88
	v_accvgpr_read_b32 v9, a89
	v_accvgpr_read_b32 v10, a90
	v_accvgpr_read_b32 v11, a91
	v_accvgpr_read_b32 v12, a92
	v_accvgpr_read_b32 v13, a93
	v_accvgpr_read_b32 v14, a94
	v_accvgpr_read_b32 v15, a95
	v_accvgpr_read_b32 v6, a32
	v_accvgpr_read_b32 v14, a40
	v_accvgpr_read_b32 v15, a41
	v_accvgpr_read_b32 v16, a42
	v_accvgpr_read_b32 v17, a43
	v_accvgpr_read_b32 v18, a44
	v_accvgpr_read_b32 v19, a45
	v_accvgpr_read_b32 v20, a46
	v_accvgpr_read_b32 v21, a47
	ds_read_b128 v[14:17], v22 offset:54016
	ds_read_b128 v[18:21], v22 offset:54080
	v_accvgpr_read_b32 v12, a38
	v_accvgpr_read_b32 v13, a39
	v_lshlrev_b32_e32 v24, 2, v85
	v_accvgpr_read_b32 v1, a81
	v_accvgpr_read_b32 v7, a33
	v_mad_i64_i32 v[12:13], s[0:1], v80, 40, s[18:19]
	v_ashrrev_i32_e32 v25, 31, v24
	v_accvgpr_read_b32 v3, a83
	v_accvgpr_read_b32 v9, a35
	v_lshl_add_u64 v[22:23], v[24:25], 2, v[12:13]
	v_mov_b32_e32 v25, v1
	s_waitcnt lgkmcnt(1)
	v_mov_b32_e32 v27, v15
	v_mov_b32_e32 v1, v7
	s_waitcnt lgkmcnt(0)
	v_mov_b32_e32 v15, v19
	v_accvgpr_read_b32 v2, a82
	v_accvgpr_read_b32 v8, a34
	v_pk_add_f32 v[0:1], v[0:1], v[14:15]
	v_mov_b32_e32 v7, v3
	v_mov_b32_e32 v15, v17
	v_mov_b32_e32 v3, v9
	v_mov_b32_e32 v17, v21
	v_mov_b32_e32 v24, v6
	v_mov_b32_e32 v26, v18
	v_mov_b32_e32 v6, v8
	v_mov_b32_e32 v14, v20
	v_pk_add_f32 v[2:3], v[2:3], v[16:17]
	v_pk_add_f32 v[24:25], v[24:25], v[26:27]
	s_waitcnt vmcnt(0)
	v_pk_mul_f32 v[0:1], v[82:83], v[0:1]
	v_pk_add_f32 v[6:7], v[6:7], v[14:15]
	v_pk_mul_f32 v[2:3], v[82:83], v[2:3]
	v_accvgpr_read_b32 v4, a84
	v_accvgpr_read_b32 v5, a85
	v_accvgpr_read_b32 v10, a36
	v_accvgpr_read_b32 v11, a37
	v_pk_fma_f32 v[0:1], v[82:83], v[24:25], v[0:1] op_sel:[1,0,0] op_sel_hi:[0,1,1]
	v_pk_fma_f32 v[2:3], v[82:83], v[6:7], v[2:3] op_sel:[1,0,0] op_sel_hi:[0,1,1]
	v_cmp_eq_u32_e32 vcc, 0, v85
	global_store_dwordx4 v[22:23], v[0:3], off
	s_and_b64 exec, exec, vcc
	s_cbranch_execz .LBB3_39
	s_mov_b32 s0, 0xd000
	v_add_u32_e64 v0, s0, 0
	ds_read2_b64 v[0:3], v0 offset0:100 offset1:108
	v_mov_b32_e32 v9, v5
	v_mov_b32_e32 v5, v11
	v_mov_b32_e32 v8, v10
	v_pk_mov_b32 v[6:7], v[82:83], v[82:83] op_sel:[1,0]
	s_waitcnt lgkmcnt(0)
	v_mov_b32_e32 v15, v1
	v_mov_b32_e32 v1, v3
	v_mov_b32_e32 v14, v2
	v_pk_add_f32 v[0:1], v[4:5], v[0:1]
	v_pk_add_f32 v[8:9], v[8:9], v[14:15]
	v_pk_mul_f32 v[0:1], v[82:83], v[0:1]
	s_nop 0
	v_pk_fma_f32 v[0:1], v[6:7], v[8:9], v[0:1]
	global_store_dwordx2 v[12:13], v[0:1], off offset:32
